# counted waits instead of compiler vmcnt(0) in four places: g_attn hoisted out of the P0 rmsnorm loop, P7 double buffer, P5 gather-offset loads consumed at the last K-iteration, fp8 conversion loop; on
# speedup vs baseline: 1.0038x; 1.0038x over previous
; __device__ __forceinline__ float shx(float v, int m, int lane) { return __int_as_float(__builtin_amdgcn_ds_bpermute((lane ^ m) << 2, __float_as_int(v))); }
; __device__ __forceinline__ unsigned pk2(float lo, float hi) { return (unsigned)f2bf(lo) | ((unsigned)f2bf(hi) << 16); }
; __device__ __forceinline__ void ph0(const Ctx& c) {
;     ...
;     bf16_t* XN = (bf16_t*)(p.ws + WS_MIXED);
;     const int gwx = (vcu - 21) * NWAVES + wave, NGWX = (G - 21) * NWAVES;
;     for (int m0 = (G > 42 ? gwx : gw) * 4; m0 < NROWS && (G <= 42 || vcu >= 21); m0 += (G > 42 ? NGWX : NGW) * 4) {
;         f32x4 v[4][4];
; #pragma unroll
;         for (int r = 0; r < 4; ++r) { const int m = m0 + r < NROWS ? m0 + r : NROWS - 1; const float* xr = m < T ? p.x + (size_t)m * DM : p.meta + (size_t)(m - T) * DM;
; #pragma unroll
;             for (int j = 0; j < 4; ++j) v[r][j] = ((const f32x4*)xr)[lane + 64 * j]; }
; #pragma unroll
;         for (int r = 0; r < 4; ++r) { const int m = m0 + r; float s = 0.f;
; #pragma unroll
;             for (int j = 0; j < 4; ++j) s += (v[r][j][0] * v[r][j][0] + v[r][j][1] * v[r][j][1]) + (v[r][j][2] * v[r][j][2] + v[r][j][3] * v[r][j][3]);
; #pragma unroll
;             for (int o = 1; o < 64; o <<= 1) s += shx(s, o, lane);
;             const float rs = rsqrtf(s * (1.0f / DM) + EPS);
;             if (m < NROWS) {
; #pragma unroll
;                 for (int j = 0; j < 4; ++j) { const f32x4 g = ((const f32x4*)p.g_attn)[lane + 64 * j]; const f32x4 y = v[r][j] * rs * g; u32x2 w; w.x = pk2(y[0], y[1]); w.y = pk2(y[2], y[3]); ((u32x2*)(XN + (size_t)m * DM))[lane + 64 * j] = w; } } }
.LBB7_116:
	s_add_i32 s6, s2, 0xffffff58
	s_cmp_gt_i32 s3, 42
	s_cselect_b64 s[0:1], -1, 0
	s_and_b64 s[4:5], s[0:1], exec
	s_cselect_b32 s2, s6, s2
	s_cmpk_gt_i32 s2, 0x4003
	s_cbranch_scc1 .LBB7_126
	s_cmp_lt_i32 s3, 43
	s_cselect_b64 s[4:5], -1, 0
	s_cmp_gt_i32 s95, 20
	s_cselect_b64 s[6:7], -1, 0
	s_or_b64 s[4:5], s[4:5], s[6:7]
	s_andn2_b64 vcc, exec, s[4:5]
	s_cbranch_vccnz .LBB7_126
	s_lshl_b32 s4, s3, 5
	s_add_i32 s5, s4, 0xfffffd60
	s_and_b64 s[0:1], s[0:1], exec
	s_cselect_b32 s4, s5, s4
	s_lshl_b32 s6, s2, 2
	s_ashr_i32 s7, s6, 31
	s_lshl_b64 s[0:1], s[6:7], 11
	s_add_u32 s0, s30, s0
	v_ashrrev_i32_e32 v1, 31, v0
	v_lshlrev_b32_e32 v2, 2, v0
	v_readlane_b32 s36, v254, 9
	s_addc_u32 s1, s31, s1
	v_xor_b32_e32 v61, 4, v2
	v_xor_b32_e32 v68, 8, v2
	v_xor_b32_e32 v69, 16, v2
	v_xor_b32_e32 v70, 32, v2
	v_xor_b32_e32 v71, 64, v2
	v_xor_b32_e32 v72, 0x80, v2
	v_readlane_b32 s40, v254, 13
	v_readlane_b32 s41, v254, 14
	v_lshl_add_u64 v[2:3], v[0:1], 3, s[0:1]
	s_mov_b64 s[0:1], 0x37000000
	s_ashr_i32 s5, s4, 31
	v_lshl_add_u64 v[62:63], v[0:1], 4, s[40:41]
	v_lshl_add_u64 v[64:65], v[2:3], 0, s[0:1]
	s_lshl_b64 s[8:9], s[4:5], 11
	s_mov_b32 s2, 0xffff0000
	v_lshlrev_b64 v[66:67], 4, v[0:1]
	v_mov_b32_e32 v73, 0x358637bd
	s_mov_b32 s10, 0x800000
	s_movk_i32 s11, 0x7fff
	s_movk_i32 s12, 0x1000
	v_readlane_b32 s37, v254, 10
	v_readlane_b32 s38, v254, 11
	v_readlane_b32 s39, v254, 12
	v_readlane_b32 s42, v254, 15
	v_readlane_b32 s43, v254, 16
	v_readlane_b32 s44, v254, 17
	v_readlane_b32 s45, v254, 18
	v_readlane_b32 s46, v254, 19
	v_readlane_b32 s47, v254, 20
	v_readlane_b32 s48, v254, 21
	v_readlane_b32 s49, v254, 22
	v_readlane_b32 s50, v254, 23
	v_readlane_b32 s51, v254, 24
	global_load_dwordx4 v[100:103], v[62:63], off
	global_load_dwordx4 v[104:107], v[62:63], off offset:1024
	global_load_dwordx4 v[108:111], v[62:63], off offset:2048
	global_load_dwordx4 v[112:115], v[62:63], off offset:3072
	s_waitcnt vmcnt(0)
	s_branch .LBB7_120

; __device__ __forceinline__ float shx(float v, int m, int lane) { return __int_as_float(__builtin_amdgcn_ds_bpermute((lane ^ m) << 2, __float_as_int(v))); }
; __device__ __forceinline__ unsigned pk2(float lo, float hi) { return (unsigned)f2bf(lo) | ((unsigned)f2bf(hi) << 16); }
; __device__ __forceinline__ void ph0(const Ctx& c) {
;     ...
;     for (int m0 = (G > 42 ? gwx : gw) * 4; m0 < NROWS && (G <= 42 || vcu >= 21); m0 += (G > 42 ? NGWX : NGW) * 4) {
;         f32x4 v[4][4];
; #pragma unroll
;         for (int r = 0; r < 4; ++r) { const int m = m0 + r < NROWS ? m0 + r : NROWS - 1; const float* xr = m < T ? p.x + (size_t)m * DM : p.meta + (size_t)(m - T) * DM;
; #pragma unroll
;             for (int j = 0; j < 4; ++j) v[r][j] = ((const f32x4*)xr)[lane + 64 * j]; }
; #pragma unroll
;         for (int r = 0; r < 4; ++r) { const int m = m0 + r; float s = 0.f;
; #pragma unroll
;             for (int j = 0; j < 4; ++j) s += (v[r][j][0] * v[r][j][0] + v[r][j][1] * v[r][j][1]) + (v[r][j][2] * v[r][j][2] + v[r][j][3] * v[r][j][3]);
; #pragma unroll
;             for (int o = 1; o < 64; o <<= 1) s += shx(s, o, lane);
;             const float rs = rsqrtf(s * (1.0f / DM) + EPS);
;             if (m < NROWS) {
; #pragma unroll
;                 for (int j = 0; j < 4; ++j) { const f32x4 g = ((const f32x4*)p.g_attn)[lane + 64 * j]; const f32x4 y = v[r][j] * rs * g; u32x2 w; w.x = pk2(y[0], y[1]); w.y = pk2(y[2], y[3]); ((u32x2*)(XN + (size_t)m * DM))[lane + 64 * j] = w; } } }
.LBB7_120:
	s_add_i32 s0, s6, 0xffff0000
	s_cmp_lt_i32 s6, 0x10000
	v_readlane_b32 s36, v254, 9
	s_cselect_b32 s1, s7, 0
	s_cselect_b32 s0, s6, s0
	v_readlane_b32 s37, v254, 10
	v_readlane_b32 s38, v254, 11
	v_readlane_b32 s39, v254, 12
	s_cselect_b32 s13, s37, s39
	s_cselect_b32 s14, s36, s38
	s_lshl_b64 s[0:1], s[0:1], 12
	s_add_u32 s0, s14, s0
	s_addc_u32 s1, s13, s1
	v_lshl_add_u64 v[0:1], s[0:1], 0, v[66:67]
	global_load_dwordx4 v[74:77], v[0:1], off nt
	global_load_dwordx4 v[56:59], v[0:1], off offset:1024 nt
	global_load_dwordx4 v[32:35], v[0:1], off offset:3072 nt
	global_load_dwordx4 v[52:55], v[0:1], off offset:2048 nt
	v_mov_b64_e32 v[78:79], v[100:101]
	v_mov_b64_e32 v[80:81], v[102:103]
	s_add_i32 s1, s6, 1
	s_min_i32 s0, s1, 0x1000f
	s_ashr_i32 s13, s0, 31
	s_add_i32 s14, s0, 0xffff0000
	s_cmp_lt_i32 s1, 0x10000
	s_cselect_b32 s15, s13, 0
	s_cselect_b32 s14, s0, s14
	s_cselect_b32 s0, s37, s39
	s_cselect_b32 s13, s36, s38
	s_lshl_b64 s[14:15], s[14:15], 12
	s_add_u32 s14, s13, s14
	s_addc_u32 s15, s0, s15
	v_lshl_add_u64 v[0:1], s[14:15], 0, v[66:67]
	global_load_dwordx4 v[48:51], v[0:1], off nt
	global_load_dwordx4 v[44:47], v[0:1], off offset:1024 nt
	global_load_dwordx4 v[40:43], v[0:1], off offset:2048 nt
	global_load_dwordx4 v[36:39], v[0:1], off offset:3072 nt
	s_add_i32 s0, s6, 2
	s_min_i32 s13, s0, 0x1000f
	s_ashr_i32 s14, s13, 31
	s_add_i32 s16, s13, 0xffff0000
	s_cmp_lt_i32 s0, 0x10000
	s_cselect_b32 s15, s14, 0
	s_cselect_b32 s14, s13, s16
	s_cselect_b32 s13, s37, s39
	s_cselect_b32 s16, s36, s38
	s_lshl_b64 s[14:15], s[14:15], 12
	s_add_u32 s14, s16, s14
	s_addc_u32 s15, s13, s15
	s_add_i32 s13, s6, 3
	v_readlane_b32 s40, v254, 13
	v_readlane_b32 s41, v254, 14
	v_readlane_b32 s42, v254, 15
	v_readlane_b32 s43, v254, 16
	v_readlane_b32 s44, v254, 17
	v_readlane_b32 s45, v254, 18
	v_readlane_b32 s46, v254, 19
	v_readlane_b32 s47, v254, 20
	v_readlane_b32 s48, v254, 21
	v_readlane_b32 s49, v254, 22
	v_readlane_b32 s50, v254, 23
	v_readlane_b32 s51, v254, 24
	s_waitcnt vmcnt(7)
	v_pk_mul_f32 v[0:1], v[76:77], v[76:77]
	v_pk_mul_f32 v[2:3], v[74:75], v[74:75]
	s_waitcnt vmcnt(6)
	v_pk_mul_f32 v[4:5], v[58:59], v[58:59]
	v_pk_mul_f32 v[6:7], v[56:57], v[56:57]
	v_pk_mov_b32 v[12:13], v[2:3], v[0:1] op_sel:[1,0]
	v_mov_b32_e32 v3, v1
	v_pk_mov_b32 v[0:1], v[6:7], v[4:5] op_sel:[1,0]
	v_mov_b32_e32 v7, v5
	s_waitcnt vmcnt(5)
	v_mul_f32_e32 v11, v32, v32
	s_waitcnt vmcnt(4)
	v_mul_f32_e32 v8, v53, v53
	v_mul_f32_e32 v10, v55, v55
	v_pk_add_f32 v[2:3], v[12:13], v[2:3]
	v_pk_add_f32 v[0:1], v[0:1], v[6:7]
	v_mul_f32_e32 v14, v33, v33
	v_mul_f32_e32 v15, v34, v34
	v_mul_f32_e32 v16, v35, v35
	v_pk_fma_f32 v[4:5], v[52:53], v[52:53], v[8:9] op_sel_hi:[1,1,0]
	v_pk_fma_f32 v[8:9], v[54:55], v[54:55], v[10:11] op_sel_hi:[1,1,0]
	v_pk_add_f32 v[2:3], v[2:3], v[2:3] op_sel:[0,1] op_sel_hi:[1,0]
	v_pk_add_f32 v[0:1], v[0:1], v[0:1] op_sel:[0,1] op_sel_hi:[1,0]
	v_mov_b32_e32 v5, v15
	v_mov_b32_e32 v9, v16
	v_mov_b32_e32 v3, v11
	v_mov_b32_e32 v1, v14
	v_pk_add_f32 v[4:5], v[4:5], v[8:9]
	v_pk_add_f32 v[0:1], v[2:3], v[0:1]
	s_nop 0
	v_pk_add_f32 v[0:1], v[0:1], v[4:5]
	s_nop 0
	v_add_f32_e32 v0, v0, v1
	ds_bpermute_b32 v1, v61, v0
	s_waitcnt lgkmcnt(0)
	v_add_f32_e32 v0, v0, v1
	ds_bpermute_b32 v1, v68, v0
	s_waitcnt lgkmcnt(0)
	v_add_f32_e32 v2, v0, v1
	ds_bpermute_b32 v3, v69, v2
	v_lshl_add_u64 v[0:1], s[14:15], 0, v[66:67]
	global_load_dwordx4 v[28:31], v[0:1], off nt
	global_load_dwordx4 v[24:27], v[0:1], off offset:1024 nt
	global_load_dwordx4 v[20:23], v[0:1], off offset:2048 nt
	global_load_dwordx4 v[16:19], v[0:1], off offset:3072 nt
	s_min_i32 s14, s13, 0x1000f
	s_waitcnt lgkmcnt(0)
	v_add_f32_e32 v2, v2, v3
	ds_bpermute_b32 v3, v70, v2
	s_ashr_i32 s15, s14, 31
	s_add_i32 s16, s14, 0xffff0000
	s_cmp_lt_i32 s13, 0x10000
	s_cselect_b32 s15, s15, 0
	s_waitcnt lgkmcnt(0)
	v_add_f32_e32 v0, v2, v3
	ds_bpermute_b32 v1, v71, v0
	s_cselect_b32 s14, s14, s16
	s_cselect_b32 s16, s37, s39
	s_cselect_b32 s17, s36, s38
	s_lshl_b64 s[14:15], s[14:15], 12
	s_waitcnt lgkmcnt(0)
	v_add_f32_e32 v2, v0, v1
	ds_bpermute_b32 v3, v72, v2
	s_add_u32 s14, s17, s14
	s_addc_u32 s15, s16, s15
	v_lshl_add_u64 v[0:1], s[14:15], 0, v[66:67]
	s_cmp_lt_i32 s1, 0x10010
	s_waitcnt lgkmcnt(0)
	v_add_f32_e32 v2, v2, v3
	v_fmamk_f32 v2, v2, 0x3a800000, v73
	v_mul_f32_e32 v3, 0x4b800000, v2
	v_cmp_gt_f32_e32 vcc, s10, v2
	s_nop 1
	v_cndmask_b32_e32 v2, v2, v3, vcc
	v_rsq_f32_e32 v82, v2
	global_load_dwordx4 v[12:15], v[0:1], off nt
	global_load_dwordx4 v[8:11], v[0:1], off offset:1024 nt
	global_load_dwordx4 v[4:7], v[0:1], off offset:2048 nt
	s_nop 0
	global_load_dwordx4 v[0:3], v[0:1], off offset:3072 nt
	v_mul_f32_e32 v83, 0x45800000, v82
	v_cndmask_b32_e32 v82, v82, v83, vcc
	v_pk_mul_f32 v[74:75], v[74:75], v[82:83] op_sel_hi:[1,0]
	v_pk_mul_f32 v[76:77], v[76:77], v[82:83] op_sel_hi:[1,0]
	s_waitcnt vmcnt(12)
	v_pk_mul_f32 v[74:75], v[78:79], v[74:75]
	v_pk_mul_f32 v[76:77], v[80:81], v[76:77]
	v_bfe_u32 v78, v74, 16, 1
	v_bfe_u32 v80, v76, 16, 1
	v_bfe_u32 v79, v75, 16, 1
	v_bfe_u32 v81, v77, 16, 1
	v_add3_u32 v74, v74, v78, s11
	v_add3_u32 v76, v76, v80, s11
	v_add3_u32 v75, v75, v79, s11
	v_add3_u32 v77, v77, v81, s11
	v_lshrrev_b32_e32 v74, 16, v74
	v_lshrrev_b32_e32 v76, 16, v76
	v_and_or_b32 v74, v75, s2, v74
	v_and_or_b32 v75, v77, s2, v76
	global_store_dwordx2 v[64:65], v[74:75], off
	v_mov_b64_e32 v[74:75], v[104:105]
	v_mov_b64_e32 v[76:77], v[106:107]
	v_pk_mul_f32 v[56:57], v[56:57], v[82:83] op_sel_hi:[1,0]
	v_pk_mul_f32 v[58:59], v[58:59], v[82:83] op_sel_hi:[1,0]
	v_pk_mul_f32 v[52:53], v[52:53], v[82:83] op_sel_hi:[1,0]
	v_pk_mul_f32 v[54:55], v[54:55], v[82:83] op_sel_hi:[1,0]
	v_pk_mul_f32 v[32:33], v[32:33], v[82:83] op_sel_hi:[1,0]
	v_pk_mul_f32 v[34:35], v[34:35], v[82:83] op_sel_hi:[1,0]
	s_waitcnt vmcnt(1)
; __device__ __forceinline__ float shx(float v, int m, int lane) { return __int_as_float(__builtin_amdgcn_ds_bpermute((lane ^ m) << 2, __float_as_int(v))); }
; __device__ __forceinline__ unsigned pk2(float lo, float hi) { return (unsigned)f2bf(lo) | ((unsigned)f2bf(hi) << 16); }
; __device__ __forceinline__ void ph0(const Ctx& c) {
;     ...
;         for (int r = 0; r < 4; ++r) { const int m = m0 + r; float s = 0.f;
; #pragma unroll
;             for (int j = 0; j < 4; ++j) s += (v[r][j][0] * v[r][j][0] + v[r][j][1] * v[r][j][1]) + (v[r][j][2] * v[r][j][2] + v[r][j][3] * v[r][j][3]);
; #pragma unroll
;             for (int o = 1; o < 64; o <<= 1) s += shx(s, o, lane);
;             const float rs = rsqrtf(s * (1.0f / DM) + EPS);
;             if (m < NROWS) {
; #pragma unroll
;                 for (int j = 0; j < 4; ++j) { const f32x4 g = ((const f32x4*)p.g_attn)[lane + 64 * j]; const f32x4 y = v[r][j] * rs * g; u32x2 w; w.x = pk2(y[0], y[1]); w.y = pk2(y[2], y[3]); ((u32x2*)(XN + (size_t)m * DM))[lane + 64 * j] = w; } } }
	v_pk_mul_f32 v[58:59], v[76:77], v[58:59]
	v_pk_mul_f32 v[56:57], v[74:75], v[56:57]
	v_bfe_u32 v76, v58, 16, 1
	v_bfe_u32 v74, v56, 16, 1
	v_bfe_u32 v75, v57, 16, 1
	v_bfe_u32 v77, v59, 16, 1
	v_add3_u32 v56, v56, v74, s11
	v_add3_u32 v58, v58, v76, s11
	v_add3_u32 v57, v57, v75, s11
	v_add3_u32 v59, v59, v77, s11
	v_lshrrev_b32_e32 v56, 16, v56
	v_lshrrev_b32_e32 v58, 16, v58
	v_and_or_b32 v56, v57, s2, v56
	v_and_or_b32 v57, v59, s2, v58
	global_store_dwordx2 v[64:65], v[56:57], off offset:512
	v_mov_b64_e32 v[56:57], v[108:109]
	v_mov_b64_e32 v[58:59], v[110:111]
	v_mul_f32_e32 v74, v41, v41
	v_mul_f32_e32 v75, v43, v43
	v_mul_f32_e32 v76, v37, v37
	v_mul_f32_e32 v77, v39, v39
	v_fmac_f32_e32 v74, v40, v40
	v_fmac_f32_e32 v75, v42, v42
	v_fmac_f32_e32 v76, v36, v36
	v_fmac_f32_e32 v77, v38, v38
	v_pk_mul_f32 v[54:55], v[58:59], v[54:55]
	v_pk_mul_f32 v[52:53], v[56:57], v[52:53]
	v_bfe_u32 v58, v54, 16, 1
	v_bfe_u32 v56, v52, 16, 1
	v_bfe_u32 v57, v53, 16, 1
	v_bfe_u32 v59, v55, 16, 1
	v_add3_u32 v52, v52, v56, s11
	v_add3_u32 v54, v54, v58, s11
	v_add3_u32 v53, v53, v57, s11
	v_add3_u32 v55, v55, v59, s11
	v_lshrrev_b32_e32 v52, 16, v52
	v_lshrrev_b32_e32 v54, 16, v54
	v_and_or_b32 v52, v53, s2, v52
	v_and_or_b32 v53, v55, s2, v54
	global_store_dwordx2 v[64:65], v[52:53], off offset:1024
	v_mov_b64_e32 v[54:55], v[112:113]
	v_mov_b64_e32 v[56:57], v[114:115]
	v_mul_f32_e32 v52, v49, v49
	v_mul_f32_e32 v53, v51, v51
	v_mul_f32_e32 v58, v45, v45
	v_mul_f32_e32 v59, v47, v47
	v_fmac_f32_e32 v52, v48, v48
	v_fmac_f32_e32 v53, v50, v50
	v_fmac_f32_e32 v58, v44, v44
	v_fmac_f32_e32 v59, v46, v46
	v_add_f32_e32 v52, v52, v53
	v_add_f32_e32 v53, v58, v59
	v_add_f32_e32 v58, v74, v75
	v_add_f32_e32 v52, v52, v53
	v_add_f32_e32 v59, v76, v77
	v_add_f32_e32 v52, v52, v58
	v_add_f32_e32 v52, v52, v59
	ds_bpermute_b32 v53, v61, v52
	s_waitcnt lgkmcnt(0)
	v_add_f32_e32 v52, v52, v53
	ds_bpermute_b32 v53, v68, v52
	s_waitcnt lgkmcnt(0)
	v_add_f32_e32 v52, v52, v53
	ds_bpermute_b32 v53, v69, v52
	s_waitcnt lgkmcnt(0)
	v_add_f32_e32 v52, v52, v53
	ds_bpermute_b32 v53, v70, v52
	s_waitcnt lgkmcnt(0)
	v_add_f32_e32 v52, v52, v53
	ds_bpermute_b32 v53, v71, v52
	s_waitcnt lgkmcnt(0)
	v_add_f32_e32 v52, v52, v53
	ds_bpermute_b32 v53, v72, v52
	v_pk_mul_f32 v[34:35], v[56:57], v[34:35]
	v_pk_mul_f32 v[32:33], v[54:55], v[32:33]
	v_bfe_u32 v56, v34, 16, 1
	v_bfe_u32 v54, v32, 16, 1
	v_bfe_u32 v55, v33, 16, 1
	v_bfe_u32 v57, v35, 16, 1
	v_add3_u32 v32, v32, v54, s11
	v_add3_u32 v34, v34, v56, s11
	v_add3_u32 v33, v33, v55, s11
	v_add3_u32 v35, v35, v57, s11
	v_lshrrev_b32_e32 v32, 16, v32
	v_lshrrev_b32_e32 v34, 16, v34
	v_and_or_b32 v32, v33, s2, v32
	v_and_or_b32 v33, v35, s2, v34
	global_store_dwordx2 v[64:65], v[32:33], off offset:1536
	s_cbranch_scc0 .LBB7_122
	v_mov_b64_e32 v[32:33], v[100:101]
	v_mov_b64_e32 v[34:35], v[102:103]
	s_waitcnt lgkmcnt(0)
	v_add_f32_e32 v52, v52, v53
	v_fmamk_f32 v52, v52, 0x3a800000, v73
	v_mul_f32_e32 v53, 0x4b800000, v52
	v_cmp_gt_f32_e32 vcc, s10, v52
	s_nop 1
	v_cndmask_b32_e32 v52, v52, v53, vcc
	v_rsq_f32_e32 v52, v52
	s_nop 0
	v_mul_f32_e32 v53, 0x45800000, v52
	v_cndmask_b32_e32 v52, v52, v53, vcc
	v_pk_mul_f32 v[48:49], v[48:49], v[52:53] op_sel_hi:[1,0]
	v_pk_mul_f32 v[50:51], v[50:51], v[52:53] op_sel_hi:[1,0]
	v_pk_mul_f32 v[44:45], v[44:45], v[52:53] op_sel_hi:[1,0]
	v_pk_mul_f32 v[46:47], v[46:47], v[52:53] op_sel_hi:[1,0]
	v_pk_mul_f32 v[40:41], v[40:41], v[52:53] op_sel_hi:[1,0]
	v_pk_mul_f32 v[42:43], v[42:43], v[52:53] op_sel_hi:[1,0]
	v_pk_mul_f32 v[36:37], v[36:37], v[52:53] op_sel_hi:[1,0]
	v_pk_mul_f32 v[38:39], v[38:39], v[52:53] op_sel_hi:[1,0]
	v_pk_mul_f32 v[34:35], v[50:51], v[34:35]
	v_pk_mul_f32 v[32:33], v[48:49], v[32:33]
	v_bfe_u32 v50, v34, 16, 1
	v_bfe_u32 v48, v32, 16, 1
	v_bfe_u32 v49, v33, 16, 1
	v_bfe_u32 v51, v35, 16, 1
	v_add3_u32 v32, v32, v48, s11
	v_add3_u32 v34, v34, v50, s11
	v_add3_u32 v33, v33, v49, s11
	v_add3_u32 v35, v35, v51, s11
	v_lshrrev_b32_e32 v32, 16, v32
	v_lshrrev_b32_e32 v34, 16, v34
	v_and_or_b32 v32, v33, s2, v32
	v_and_or_b32 v33, v35, s2, v34
	global_store_dwordx2 v[64:65], v[32:33], off offset:2048
	v_mov_b64_e32 v[32:33], v[104:105]
	v_mov_b64_e32 v[34:35], v[106:107]
	v_pk_mul_f32 v[34:35], v[46:47], v[34:35]
	v_pk_mul_f32 v[32:33], v[44:45], v[32:33]
	v_bfe_u32 v46, v34, 16, 1
	v_bfe_u32 v44, v32, 16, 1
	v_bfe_u32 v45, v33, 16, 1
	v_bfe_u32 v47, v35, 16, 1
	v_add3_u32 v32, v32, v44, s11
	v_add3_u32 v34, v34, v46, s11
	v_add3_u32 v33, v33, v45, s11
	v_add3_u32 v35, v35, v47, s11
	v_lshrrev_b32_e32 v32, 16, v32
	v_lshrrev_b32_e32 v34, 16, v34
	v_and_or_b32 v32, v33, s2, v32
	v_and_or_b32 v33, v35, s2, v34
	global_store_dwordx2 v[64:65], v[32:33], off offset:2560
	v_mov_b64_e32 v[32:33], v[108:109]
	v_mov_b64_e32 v[34:35], v[110:111]
	v_pk_mul_f32 v[34:35], v[42:43], v[34:35]
	v_pk_mul_f32 v[32:33], v[40:41], v[32:33]
	v_bfe_u32 v42, v34, 16, 1
	v_bfe_u32 v40, v32, 16, 1
	v_bfe_u32 v41, v33, 16, 1
	v_bfe_u32 v43, v35, 16, 1
	v_add3_u32 v32, v32, v40, s11
	v_add3_u32 v34, v34, v42, s11
	v_add3_u32 v33, v33, v41, s11
	v_add3_u32 v35, v35, v43, s11
	v_lshrrev_b32_e32 v32, 16, v32
	v_lshrrev_b32_e32 v34, 16, v34
	v_and_or_b32 v32, v33, s2, v32
	v_and_or_b32 v33, v35, s2, v34
	global_store_dwordx2 v[64:65], v[32:33], off offset:3072
	v_mov_b64_e32 v[32:33], v[112:113]
	v_mov_b64_e32 v[34:35], v[114:115]
	v_pk_mul_f32 v[34:35], v[38:39], v[34:35]
	v_pk_mul_f32 v[32:33], v[36:37], v[32:33]
	v_bfe_u32 v38, v34, 16, 1
	v_bfe_u32 v36, v32, 16, 1
	v_bfe_u32 v37, v33, 16, 1
	v_bfe_u32 v39, v35, 16, 1
	v_add3_u32 v32, v32, v36, s11
	v_add3_u32 v34, v34, v38, s11
	v_add3_u32 v33, v33, v37, s11
	v_add3_u32 v35, v35, v39, s11
	v_lshrrev_b32_e32 v32, 16, v32
	v_lshrrev_b32_e32 v34, 16, v34
	v_and_or_b32 v32, v33, s2, v32
	v_and_or_b32 v33, v35, s2, v34
	global_store_dwordx2 v[64:65], v[32:33], off offset:3584
; __device__ __forceinline__ float shx(float v, int m, int lane) { return __int_as_float(__builtin_amdgcn_ds_bpermute((lane ^ m) << 2, __float_as_int(v))); }
; __device__ __forceinline__ unsigned pk2(float lo, float hi) { return (unsigned)f2bf(lo) | ((unsigned)f2bf(hi) << 16); }
; __device__ __forceinline__ void ph0(const Ctx& c) {
;     ...
;         for (int r = 0; r < 4; ++r) { const int m = m0 + r; float s = 0.f;
; #pragma unroll
;             for (int j = 0; j < 4; ++j) s += (v[r][j][0] * v[r][j][0] + v[r][j][1] * v[r][j][1]) + (v[r][j][2] * v[r][j][2] + v[r][j][3] * v[r][j][3]);
; #pragma unroll
;             for (int o = 1; o < 64; o <<= 1) s += shx(s, o, lane);
;             const float rs = rsqrtf(s * (1.0f / DM) + EPS);
;             if (m < NROWS) {
; #pragma unroll
;                 for (int j = 0; j < 4; ++j) { const f32x4 g = ((const f32x4*)p.g_attn)[lane + 64 * j]; const f32x4 y = v[r][j] * rs * g; u32x2 w; w.x = pk2(y[0], y[1]); w.y = pk2(y[2], y[3]); ((u32x2*)(XN + (size_t)m * DM))[lane + 64 * j] = w; } } }
.LBB7_122:
	v_mul_f32_e32 v32, v29, v29
	v_mul_f32_e32 v33, v31, v31
	v_fmac_f32_e32 v32, v28, v28
	v_fmac_f32_e32 v33, v30, v30
	v_add_f32_e32 v32, v32, v33
	v_mul_f32_e32 v33, v25, v25
	v_mul_f32_e32 v34, v27, v27
	v_fmac_f32_e32 v33, v24, v24
	v_fmac_f32_e32 v34, v26, v26
	v_add_f32_e32 v33, v33, v34
	v_add_f32_e32 v32, v32, v33
	v_mul_f32_e32 v33, v21, v21
	v_mul_f32_e32 v34, v23, v23
	v_fmac_f32_e32 v33, v20, v20
	v_fmac_f32_e32 v34, v22, v22
	v_add_f32_e32 v33, v33, v34
	v_add_f32_e32 v32, v32, v33
	v_mul_f32_e32 v33, v17, v17
	v_mul_f32_e32 v34, v19, v19
	v_fmac_f32_e32 v33, v16, v16
	v_fmac_f32_e32 v34, v18, v18
	v_add_f32_e32 v33, v33, v34
	v_add_f32_e32 v32, v32, v33
	ds_bpermute_b32 v33, v61, v32
	s_cmp_gt_i32 s0, 0x1000f
	s_waitcnt lgkmcnt(0)
	v_add_f32_e32 v32, v32, v33
	ds_bpermute_b32 v33, v68, v32
	s_waitcnt lgkmcnt(0)
	v_add_f32_e32 v32, v32, v33
	ds_bpermute_b32 v33, v69, v32
	s_waitcnt lgkmcnt(0)
	v_add_f32_e32 v32, v32, v33
	ds_bpermute_b32 v33, v70, v32
	s_waitcnt lgkmcnt(0)
	v_add_f32_e32 v32, v32, v33
	ds_bpermute_b32 v33, v71, v32
	s_waitcnt lgkmcnt(0)
	v_add_f32_e32 v32, v32, v33
	ds_bpermute_b32 v33, v72, v32
	s_cbranch_scc1 .LBB7_124
	v_mov_b64_e32 v[34:35], v[100:101]
	v_mov_b64_e32 v[36:37], v[102:103]
	s_waitcnt lgkmcnt(0)
	v_add_f32_e32 v32, v32, v33
	v_fmamk_f32 v32, v32, 0x3a800000, v73
	v_mul_f32_e32 v33, 0x4b800000, v32
	v_cmp_gt_f32_e32 vcc, s10, v32
	s_nop 1
	v_cndmask_b32_e32 v32, v32, v33, vcc
	v_rsq_f32_e32 v38, v32
	v_add_co_u32_e64 v32, s[0:1], s12, v64
	v_mul_f32_e32 v39, 0x45800000, v38
	v_cndmask_b32_e32 v38, v38, v39, vcc
	v_pk_mul_f32 v[28:29], v[28:29], v[38:39] op_sel_hi:[1,0]
	v_pk_mul_f32 v[30:31], v[30:31], v[38:39] op_sel_hi:[1,0]
	v_addc_co_u32_e64 v33, s[0:1], 0, v65, s[0:1]
	v_pk_mul_f32 v[24:25], v[24:25], v[38:39] op_sel_hi:[1,0]
	v_pk_mul_f32 v[26:27], v[26:27], v[38:39] op_sel_hi:[1,0]
	v_pk_mul_f32 v[20:21], v[20:21], v[38:39] op_sel_hi:[1,0]
	v_pk_mul_f32 v[22:23], v[22:23], v[38:39] op_sel_hi:[1,0]
	v_pk_mul_f32 v[16:17], v[16:17], v[38:39] op_sel_hi:[1,0]
	v_pk_mul_f32 v[18:19], v[18:19], v[38:39] op_sel_hi:[1,0]
	v_pk_mul_f32 v[30:31], v[30:31], v[36:37]
	v_pk_mul_f32 v[28:29], v[28:29], v[34:35]
	v_bfe_u32 v36, v30, 16, 1
	v_bfe_u32 v34, v28, 16, 1
	v_bfe_u32 v35, v29, 16, 1
	v_bfe_u32 v37, v31, 16, 1
	v_add3_u32 v28, v28, v34, s11
	v_add3_u32 v30, v30, v36, s11
	v_add3_u32 v29, v29, v35, s11
	v_add3_u32 v31, v31, v37, s11
	v_lshrrev_b32_e32 v28, 16, v28
	v_lshrrev_b32_e32 v30, 16, v30
	v_and_or_b32 v28, v29, s2, v28
	v_and_or_b32 v29, v31, s2, v30
	global_store_dwordx2 v[32:33], v[28:29], off
	v_mov_b64_e32 v[28:29], v[104:105]
	v_mov_b64_e32 v[30:31], v[106:107]
	v_pk_mul_f32 v[26:27], v[26:27], v[30:31]
	v_pk_mul_f32 v[24:25], v[24:25], v[28:29]
	v_bfe_u32 v30, v26, 16, 1
	v_bfe_u32 v28, v24, 16, 1
	v_bfe_u32 v29, v25, 16, 1
	v_bfe_u32 v31, v27, 16, 1
	v_add3_u32 v24, v24, v28, s11
	v_add3_u32 v26, v26, v30, s11
	v_add3_u32 v25, v25, v29, s11
	v_add3_u32 v27, v27, v31, s11
	v_lshrrev_b32_e32 v24, 16, v24
	v_lshrrev_b32_e32 v26, 16, v26
	v_and_or_b32 v24, v25, s2, v24
	v_and_or_b32 v25, v27, s2, v26
	global_store_dwordx2 v[32:33], v[24:25], off offset:512
	v_mov_b64_e32 v[24:25], v[108:109]
	v_mov_b64_e32 v[26:27], v[110:111]
	v_pk_mul_f32 v[22:23], v[22:23], v[26:27]
	v_pk_mul_f32 v[20:21], v[20:21], v[24:25]
	v_bfe_u32 v26, v22, 16, 1
	v_bfe_u32 v24, v20, 16, 1
	v_bfe_u32 v25, v21, 16, 1
	v_bfe_u32 v27, v23, 16, 1
	v_add3_u32 v20, v20, v24, s11
	v_add3_u32 v22, v22, v26, s11
	v_add3_u32 v21, v21, v25, s11
	v_add3_u32 v23, v23, v27, s11
	v_lshrrev_b32_e32 v20, 16, v20
	v_lshrrev_b32_e32 v22, 16, v22
	v_and_or_b32 v20, v21, s2, v20
	v_and_or_b32 v21, v23, s2, v22
	global_store_dwordx2 v[32:33], v[20:21], off offset:1024
	v_mov_b64_e32 v[20:21], v[112:113]
	v_mov_b64_e32 v[22:23], v[114:115]
	v_pk_mul_f32 v[18:19], v[18:19], v[22:23]
	v_pk_mul_f32 v[16:17], v[16:17], v[20:21]
	v_bfe_u32 v22, v18, 16, 1
	v_bfe_u32 v20, v16, 16, 1
	v_bfe_u32 v21, v17, 16, 1
	v_bfe_u32 v23, v19, 16, 1
	v_add3_u32 v16, v16, v20, s11
	v_add3_u32 v18, v18, v22, s11
	v_add3_u32 v17, v17, v21, s11
	v_add3_u32 v19, v19, v23, s11
	v_lshrrev_b32_e32 v16, 16, v16
	v_lshrrev_b32_e32 v18, 16, v18
	v_and_or_b32 v16, v17, s2, v16
	v_and_or_b32 v17, v19, s2, v18
	global_store_dwordx2 v[32:33], v[16:17], off offset:1536
; __device__ __forceinline__ float shx(float v, int m, int lane) { return __int_as_float(__builtin_amdgcn_ds_bpermute((lane ^ m) << 2, __float_as_int(v))); }
; __device__ __forceinline__ unsigned pk2(float lo, float hi) { return (unsigned)f2bf(lo) | ((unsigned)f2bf(hi) << 16); }
; __device__ __forceinline__ void ph0(const Ctx& c) {
;     ...
;         for (int r = 0; r < 4; ++r) { const int m = m0 + r; float s = 0.f;
; #pragma unroll
;             for (int j = 0; j < 4; ++j) s += (v[r][j][0] * v[r][j][0] + v[r][j][1] * v[r][j][1]) + (v[r][j][2] * v[r][j][2] + v[r][j][3] * v[r][j][3]);
; #pragma unroll
;             for (int o = 1; o < 64; o <<= 1) s += shx(s, o, lane);
;             const float rs = rsqrtf(s * (1.0f / DM) + EPS);
;             if (m < NROWS) {
; #pragma unroll
;                 for (int j = 0; j < 4; ++j) { const f32x4 g = ((const f32x4*)p.g_attn)[lane + 64 * j]; const f32x4 y = v[r][j] * rs * g; u32x2 w; w.x = pk2(y[0], y[1]); w.y = pk2(y[2], y[3]); ((u32x2*)(XN + (size_t)m * DM))[lane + 64 * j] = w; } } }
.LBB7_124:
	v_mul_f32_e32 v16, v13, v13
	v_mul_f32_e32 v17, v15, v15
	v_fmac_f32_e32 v16, v12, v12
	v_fmac_f32_e32 v17, v14, v14
	v_add_f32_e32 v16, v16, v17
	v_mul_f32_e32 v17, v9, v9
	v_mul_f32_e32 v18, v11, v11
	v_fmac_f32_e32 v17, v8, v8
	v_fmac_f32_e32 v18, v10, v10
	v_add_f32_e32 v17, v17, v18
	v_add_f32_e32 v16, v16, v17
	v_mul_f32_e32 v17, v5, v5
	v_mul_f32_e32 v18, v7, v7
	v_fmac_f32_e32 v17, v4, v4
	v_fmac_f32_e32 v18, v6, v6
	v_add_f32_e32 v17, v17, v18
	v_add_f32_e32 v16, v16, v17
	v_mul_f32_e32 v17, v1, v1
	v_mul_f32_e32 v18, v3, v3
	v_fmac_f32_e32 v17, v0, v0
	v_fmac_f32_e32 v18, v2, v2
	v_add_f32_e32 v17, v17, v18
	v_add_f32_e32 v16, v16, v17
	ds_bpermute_b32 v17, v61, v16
	s_cmp_gt_i32 s13, 0x1000f
	s_waitcnt lgkmcnt(0)
	v_add_f32_e32 v16, v16, v17
	ds_bpermute_b32 v17, v68, v16
	s_waitcnt lgkmcnt(0)
	v_add_f32_e32 v16, v16, v17
	ds_bpermute_b32 v17, v69, v16
	s_waitcnt lgkmcnt(0)
	v_add_f32_e32 v16, v16, v17
	ds_bpermute_b32 v17, v70, v16
	s_waitcnt lgkmcnt(0)
	v_add_f32_e32 v16, v16, v17
	ds_bpermute_b32 v17, v71, v16
	s_waitcnt lgkmcnt(0)
	v_add_f32_e32 v16, v16, v17
	ds_bpermute_b32 v17, v72, v16
	s_cbranch_scc1 .LBB7_119
	v_mov_b64_e32 v[18:19], v[100:101]
	v_mov_b64_e32 v[20:21], v[102:103]
	s_waitcnt lgkmcnt(0)
	v_add_f32_e32 v16, v16, v17
	v_fmamk_f32 v16, v16, 0x3a800000, v73
	v_mul_f32_e32 v17, 0x4b800000, v16
	v_cmp_gt_f32_e32 vcc, s10, v16
	s_nop 1
	v_cndmask_b32_e32 v16, v16, v17, vcc
	v_rsq_f32_e32 v22, v16
	v_add_co_u32_e64 v16, s[0:1], s12, v64
	v_mul_f32_e32 v23, 0x45800000, v22
	v_cndmask_b32_e32 v22, v22, v23, vcc
	v_pk_mul_f32 v[12:13], v[12:13], v[22:23] op_sel_hi:[1,0]
	v_pk_mul_f32 v[14:15], v[14:15], v[22:23] op_sel_hi:[1,0]
	v_addc_co_u32_e64 v17, s[0:1], 0, v65, s[0:1]
	v_pk_mul_f32 v[8:9], v[8:9], v[22:23] op_sel_hi:[1,0]
	v_pk_mul_f32 v[10:11], v[10:11], v[22:23] op_sel_hi:[1,0]
	v_pk_mul_f32 v[4:5], v[4:5], v[22:23] op_sel_hi:[1,0]
	v_pk_mul_f32 v[6:7], v[6:7], v[22:23] op_sel_hi:[1,0]
	v_pk_mul_f32 v[0:1], v[0:1], v[22:23] op_sel_hi:[1,0]
	v_pk_mul_f32 v[2:3], v[2:3], v[22:23] op_sel_hi:[1,0]
	v_pk_mul_f32 v[14:15], v[14:15], v[20:21]
	v_pk_mul_f32 v[12:13], v[12:13], v[18:19]
	v_bfe_u32 v20, v14, 16, 1
	v_bfe_u32 v18, v12, 16, 1
	v_bfe_u32 v19, v13, 16, 1
	v_bfe_u32 v21, v15, 16, 1
	v_add3_u32 v12, v12, v18, s11
	v_add3_u32 v14, v14, v20, s11
	v_add3_u32 v13, v13, v19, s11
	v_add3_u32 v15, v15, v21, s11
	v_lshrrev_b32_e32 v12, 16, v12
	v_lshrrev_b32_e32 v14, 16, v14
	v_and_or_b32 v12, v13, s2, v12
	v_and_or_b32 v13, v15, s2, v14
	global_store_dwordx2 v[16:17], v[12:13], off offset:2048
	v_mov_b64_e32 v[12:13], v[104:105]
	v_mov_b64_e32 v[14:15], v[106:107]
	v_pk_mul_f32 v[10:11], v[10:11], v[14:15]
	v_pk_mul_f32 v[8:9], v[8:9], v[12:13]
	v_bfe_u32 v14, v10, 16, 1
	v_bfe_u32 v12, v8, 16, 1
	v_bfe_u32 v13, v9, 16, 1
	v_bfe_u32 v15, v11, 16, 1
	v_add3_u32 v8, v8, v12, s11
	v_add3_u32 v10, v10, v14, s11
	v_add3_u32 v9, v9, v13, s11
	v_add3_u32 v11, v11, v15, s11
	v_lshrrev_b32_e32 v8, 16, v8
	v_lshrrev_b32_e32 v10, 16, v10
	v_and_or_b32 v8, v9, s2, v8
	v_and_or_b32 v9, v11, s2, v10
	global_store_dwordx2 v[16:17], v[8:9], off offset:2560
	v_mov_b64_e32 v[8:9], v[108:109]
	v_mov_b64_e32 v[10:11], v[110:111]
	v_pk_mul_f32 v[6:7], v[6:7], v[10:11]
	v_pk_mul_f32 v[4:5], v[4:5], v[8:9]
	v_bfe_u32 v10, v6, 16, 1
	v_bfe_u32 v8, v4, 16, 1
	v_bfe_u32 v9, v5, 16, 1
	v_bfe_u32 v11, v7, 16, 1
	v_add3_u32 v4, v4, v8, s11
	v_add3_u32 v6, v6, v10, s11
	v_add3_u32 v5, v5, v9, s11
	v_add3_u32 v7, v7, v11, s11
	v_lshrrev_b32_e32 v4, 16, v4
	v_lshrrev_b32_e32 v6, 16, v6
	v_and_or_b32 v4, v5, s2, v4
	v_and_or_b32 v5, v7, s2, v6
	global_store_dwordx2 v[16:17], v[4:5], off offset:3072
	v_mov_b64_e32 v[4:5], v[112:113]
	v_mov_b64_e32 v[6:7], v[114:115]
	v_pk_mul_f32 v[2:3], v[2:3], v[6:7]
	v_pk_mul_f32 v[0:1], v[0:1], v[4:5]
	v_bfe_u32 v6, v2, 16, 1
	v_bfe_u32 v4, v0, 16, 1
	v_bfe_u32 v5, v1, 16, 1
	v_bfe_u32 v7, v3, 16, 1
	v_add3_u32 v0, v0, v4, s11
	v_add3_u32 v2, v2, v6, s11
	v_add3_u32 v1, v1, v5, s11
	v_add3_u32 v3, v3, v7, s11
	v_lshrrev_b32_e32 v0, 16, v0
	v_lshrrev_b32_e32 v2, 16, v2
	v_and_or_b32 v0, v1, s2, v0
	v_and_or_b32 v1, v3, s2, v2
	global_store_dwordx2 v[16:17], v[0:1], off offset:3584
	s_branch .LBB7_119

; __device__ __forceinline__ F8Item f8_item(const P& p, int r) {
;     constexpr int I_W1 = 8 * 64, I_W2 = 8 * 32; F8Item it;
;     if (r < NE * I_W1) { const int e = r / I_W1, q = r % I_W1; it.W = p.w1 + (size_t)e * DM * 2048; it.WT = p.ws + WS_W1T + (size_t)e * 2048 * DM; it.N = 2048; it.k0 = 128 * (q / 64); it.n0 = 32 * (q % 64); it.map = 1; }
;     else { r -= NE * I_W1; const int e = r / I_W2, q = r % I_W2; it.W = p.w2 + (size_t)e * DM * DM; it.WT = p.ws + WS_W2T + (size_t)e * DM * DM; it.N = DM; it.k0 = 128 * (q / 32); it.n0 = 32 * (q % 32); it.map = 0; }
;     return it;
; }
; __device__ __forceinline__ void f8_load(const F8Item& it, f32x4 (&v)[16], int lane) {
; #pragma unroll
;     for (int i = 0; i < 16; ++i) v[i] = *(const f32x4*)(it.W + (size_t)(it.k0 + 32 * (i >> 2) + 4 * (lane >> 3) + (i & 3)) * it.N + it.n0 + 4 * (lane & 7));
; }
; __device__ __forceinline__ void f8_share(const P& p, LAS unsigned char* ring, int G, int vcu, int wave) {
;     ...
;     F8Item ia = f8_item(p, it < NF8 ? it : 0), ib = ia;
;     if (it < NF8) f8_load(ia, va, lane);
;     if (it + NGW < NF8) { ib = f8_item(p, it + NGW); f8_load(ib, vb, lane); }
.LBB7_401:
	v_readlane_b32 s58, v254, 53
	s_andn2_b64 vcc, exec, s[70:71]
	v_mov_b32_e32 v211, v164
	s_mov_b32 s36, s12
	s_mov_b32 s56, s5
	v_readlane_b32 s59, v254, 54
	s_cbranch_vccnz .Lf8a_pre_skip_b
	v_add_u32_e32 v120, s67, v159
	v_add_u32_e32 v122, s67, v169
	v_ashrrev_i32_e32 v121, 31, v120
	v_ashrrev_i32_e32 v123, 31, v122
	v_lshlrev_b64 v[56:57], s52, v[120:121]
	v_or_b32_e32 v58, 1, v120
	s_waitcnt vmcnt(16)
	v_or_b32_e32 v72, 2, v120
	v_lshlrev_b64 v[74:75], s52, v[122:123]
	v_add_u32_e32 v80, 32, v120
	v_add_u32_e32 v82, 33, v120
	v_add_u32_e32 v88, 34, v120
	v_add_u32_e32 v90, 32, v122
	v_add_u32_e32 v96, 64, v120
	v_add_u32_e32 v98, 0x41, v120
	v_add_u32_e32 v104, 0x42, v120
	v_add_u32_e32 v106, 64, v122
	v_add_u32_e32 v112, 0x60, v120
	v_add_u32_e32 v114, 0x61, v120
	v_add_u32_e32 v120, 0x62, v120
	v_add_u32_e32 v122, 0x60, v122
	v_ashrrev_i32_e32 v59, 31, v58
	v_ashrrev_i32_e32 v73, 31, v72
	v_ashrrev_i32_e32 v81, 31, v80
	v_ashrrev_i32_e32 v83, 31, v82
	v_ashrrev_i32_e32 v89, 31, v88
	v_ashrrev_i32_e32 v91, 31, v90
	v_ashrrev_i32_e32 v97, 31, v96
	v_ashrrev_i32_e32 v99, 31, v98
	v_ashrrev_i32_e32 v105, 31, v104
	v_ashrrev_i32_e32 v107, 31, v106
	v_ashrrev_i32_e32 v113, 31, v112
	v_ashrrev_i32_e32 v115, 31, v114
	v_ashrrev_i32_e32 v121, 31, v120
	v_ashrrev_i32_e32 v123, 31, v122
	v_lshlrev_b64 v[58:59], s52, v[58:59]
	v_lshlrev_b64 v[72:73], s52, v[72:73]
	v_lshlrev_b64 v[80:81], s52, v[80:81]
	v_lshlrev_b64 v[82:83], s52, v[82:83]
	v_lshlrev_b64 v[88:89], s52, v[88:89]
	v_lshlrev_b64 v[90:91], s52, v[90:91]
	v_lshlrev_b64 v[96:97], s52, v[96:97]
	v_lshlrev_b64 v[98:99], s52, v[98:99]
	v_lshlrev_b64 v[104:105], s52, v[104:105]
	v_lshlrev_b64 v[106:107], s52, v[106:107]
	v_lshlrev_b64 v[112:113], s52, v[112:113]
	v_lshlrev_b64 v[114:115], s52, v[114:115]
	v_lshlrev_b64 v[120:121], s52, v[120:121]
	v_lshlrev_b64 v[122:123], s52, v[122:123]
	v_lshl_add_u64 v[56:57], v[56:57], 2, s[44:45]
	v_lshl_add_u64 v[58:59], v[58:59], 2, s[44:45]
	v_lshl_add_u64 v[72:73], v[72:73], 2, s[44:45]
	v_lshl_add_u64 v[74:75], v[74:75], 2, s[44:45]
	v_lshl_add_u64 v[80:81], v[80:81], 2, s[44:45]
	v_lshl_add_u64 v[82:83], v[82:83], 2, s[44:45]
	v_lshl_add_u64 v[88:89], v[88:89], 2, s[44:45]
	v_lshl_add_u64 v[90:91], v[90:91], 2, s[44:45]
	v_lshl_add_u64 v[96:97], v[96:97], 2, s[44:45]
	v_lshl_add_u64 v[98:99], v[98:99], 2, s[44:45]
	v_lshl_add_u64 v[104:105], v[104:105], 2, s[44:45]
	v_lshl_add_u64 v[106:107], v[106:107], 2, s[44:45]
	v_lshl_add_u64 v[112:113], v[112:113], 2, s[44:45]
	v_lshl_add_u64 v[114:115], v[114:115], 2, s[44:45]
	v_lshl_add_u64 v[120:121], v[120:121], 2, s[44:45]
	v_lshl_add_u64 v[122:123], v[122:123], 2, s[44:45]
	v_lshl_add_u64 v[56:57], v[56:57], 0, v[156:157]
	v_lshl_add_u64 v[60:61], v[58:59], 0, v[156:157]
	v_lshl_add_u64 v[72:73], v[72:73], 0, v[156:157]
	v_lshl_add_u64 v[76:77], v[74:75], 0, v[156:157]
	v_lshl_add_u64 v[80:81], v[80:81], 0, v[156:157]
	v_lshl_add_u64 v[84:85], v[82:83], 0, v[156:157]
	v_lshl_add_u64 v[88:89], v[88:89], 0, v[156:157]
	v_lshl_add_u64 v[92:93], v[90:91], 0, v[156:157]
	v_lshl_add_u64 v[96:97], v[96:97], 0, v[156:157]
	v_lshl_add_u64 v[100:101], v[98:99], 0, v[156:157]
	v_lshl_add_u64 v[104:105], v[104:105], 0, v[156:157]
	v_lshl_add_u64 v[108:109], v[106:107], 0, v[156:157]
	v_lshl_add_u64 v[112:113], v[112:113], 0, v[156:157]
	v_lshl_add_u64 v[116:117], v[114:115], 0, v[156:157]
	v_lshl_add_u64 v[120:121], v[120:121], 0, v[156:157]
	v_lshl_add_u64 v[124:125], v[122:123], 0, v[156:157]
	global_load_dwordx4 v[56:59], v[56:57], off
	s_nop 0
	global_load_dwordx4 v[60:63], v[60:61], off
	s_nop 0
	global_load_dwordx4 v[72:75], v[72:73], off
	s_nop 0
	global_load_dwordx4 v[76:79], v[76:77], off
	s_nop 0
	global_load_dwordx4 v[80:83], v[80:81], off
	s_nop 0
	global_load_dwordx4 v[84:87], v[84:85], off
	s_nop 0
	global_load_dwordx4 v[88:91], v[88:89], off
	s_nop 0
	global_load_dwordx4 v[92:95], v[92:93], off
	s_nop 0
	global_load_dwordx4 v[96:99], v[96:97], off
	s_nop 0
	global_load_dwordx4 v[100:103], v[100:101], off
	s_nop 0
	global_load_dwordx4 v[104:107], v[104:105], off
	s_nop 0
	global_load_dwordx4 v[108:111], v[108:109], off
	s_nop 0
	global_load_dwordx4 v[112:115], v[112:113], off
	s_nop 0
	global_load_dwordx4 v[116:119], v[116:117], off
	s_nop 0
	global_load_dwordx4 v[120:123], v[120:121], off
	s_nop 0
	global_load_dwordx4 v[124:127], v[124:125], off
	v_readlane_b32 s10, v255, 2
	v_readlane_b32 s58, v255, 0
	v_mov_b32_e32 v211, v165
	s_mov_b32 s36, s10
	s_mov_b32 s56, s67
	v_readlane_b32 s59, v255, 1
	v_readlane_b32 s11, v255, 3
; #define LAS __attribute__((address_space(3)))
; #define LDS_WAIT() asm volatile("s_waitcnt lgkmcnt(0)" ::: "memory")
; __device__ __forceinline__ int rmap_w2(int c) { const int cc = c & 255; return (c & ~255) + 128 * ((cc >> 3) & 1) + 32 * (cc >> 6) + 8 * ((cc >> 4) & 3) + (cc & 7); }
; __device__ __forceinline__ float cl448(float v) { return fminf(fmaxf(v, -448.0f), 448.0f); }
; __device__ __forceinline__ void f8_pack(const f32x4 (&v)[16], LAS float* scr, int lane) {
;     LAS unsigned* su = (LAS unsigned*)scr; const int nq = lane & 7, kg = lane >> 3;
; #pragma unroll
;     for (int i2 = 0; i2 < 4; ++i2)
; #pragma unroll
;         for (int x = 0; x < 4; ++x) { const int r = 4 * nq + x, chunk = 2 * i2 + (kg >> 2);
;             su[r * 32 + ((chunk ^ (r & 7)) << 2) + (kg & 3)] = pg8::pk4_fp8(cl448(8.0f * v[4 * i2][x]), cl448(8.0f * v[4 * i2 + 1][x]), cl448(8.0f * v[4 * i2 + 2][x]), cl448(8.0f * v[4 * i2 + 3][x])); }
;     LDS_WAIT(); asm volatile("" ::: "memory");
; }
; __device__ __forceinline__ void f8_store(const F8Item& it, LAS float* scr, int lane) {
;     const LAS unsigned* su = (const LAS unsigned*)scr; const int n = lane >> 1, half = lane & 1;
;     u32x4 o[4];
; #pragma unroll
;     for (int q = 0; q < 4; ++q) o[q] = *(const LAS u32x4*)(su + n * 32 + (((4 * half + q) ^ (n & 7)) << 2));
;     const int src = it.n0 + n; const int row = it.map ? rmap_w1(src) : rmap_w2(src); unsigned char* dst = it.WT + (size_t)row * DM + it.k0 + 64 * half;
; __device__ __forceinline__ void f8_share(const P& p, LAS unsigned char* ring, int G, int vcu, int wave) {
;     ...
;     while (it < NF8) {
;         { const F8Item cur = ia; f8_pack(va, scr, lane); if (it + 2 * NGW < NF8) { ia = f8_item(p, it + 2 * NGW); f8_load(ia, va, lane); } f8_store(cur, scr, lane); }
.LBB7_403:
	s_and_b64 vcc, exec, s[0:1]
	s_cbranch_vccnz .LBB7_432
	v_lshlrev_b32_e32 v129, 2, v128
	v_ashrrev_i32_e32 v130, 5, v128
	v_and_b32_e32 v144, 28, v129
	v_bitop3_b32 v131, v129, v130, 4 bitop3:0x6c
	v_lshrrev_b32_e32 v133, 1, v128
	v_lshl_add_u32 v132, v144, 7, s86
	v_lshlrev_b32_e32 v131, 4, v131
	v_and_b32_e32 v133, 12, v133
	v_add3_u32 v170, v132, v131, v133
	v_or_b32_e32 v131, 1, v144
	v_bitop3_b32 v134, v131, v130, 5 bitop3:0x6c
	v_lshl_add_u32 v135, v131, 7, s86
	v_lshlrev_b32_e32 v134, 4, v134
	v_add3_u32 v171, v135, v134, v133
	v_or_b32_e32 v134, 2, v144
	v_bitop3_b32 v136, v134, v130, 6 bitop3:0x6c
	v_lshl_add_u32 v137, v134, 7, s86
	v_lshlrev_b32_e32 v136, 4, v136
	v_add3_u32 v179, v137, v136, v133
	v_or_b32_e32 v136, 3, v144
	v_bitop3_b32 v138, v136, v130, 7 bitop3:0x6c
	v_lshl_add_u32 v139, v136, 7, s86
	v_lshlrev_b32_e32 v138, 4, v138
	v_add3_u32 v180, v139, v138, v133
	v_add_u32_e32 v138, 2, v130
	v_bitop3_b32 v140, v129, v138, 4 bitop3:0x6c
	v_lshlrev_b32_e32 v140, 4, v140
	v_add3_u32 v181, v132, v140, v133
	v_bitop3_b32 v140, v131, v138, 5 bitop3:0x6c
	v_lshlrev_b32_e32 v140, 4, v140
	v_add3_u32 v182, v135, v140, v133
	v_bitop3_b32 v140, v134, v138, 6 bitop3:0x6c
	v_bitop3_b32 v138, v136, v138, 7 bitop3:0x6c
	v_lshlrev_b32_e32 v138, 4, v138
	v_lshlrev_b32_e32 v140, 4, v140
	v_add3_u32 v184, v139, v138, v133
	v_add_u32_e32 v138, 4, v130
	v_add_u32_e32 v130, 6, v130
	v_add3_u32 v183, v137, v140, v133
	v_bitop3_b32 v140, v129, v138, 4 bitop3:0x6c
	v_bitop3_b32 v129, v129, v130, 4 bitop3:0x6c
	v_lshlrev_b32_e32 v129, 4, v129
	v_add3_u32 v189, v132, v129, v133
	v_bitop3_b32 v129, v131, v130, 5 bitop3:0x6c
	v_lshlrev_b32_e32 v140, 4, v140
	v_lshlrev_b32_e32 v129, 4, v129
	v_add3_u32 v185, v132, v140, v133
	v_bitop3_b32 v140, v131, v138, 5 bitop3:0x6c
	v_add3_u32 v190, v135, v129, v133
	v_bitop3_b32 v129, v134, v130, 6 bitop3:0x6c
	v_lshlrev_b32_e32 v140, 4, v140
	v_lshlrev_b32_e32 v129, 4, v129
	v_add3_u32 v186, v135, v140, v133
	v_bitop3_b32 v140, v134, v138, 6 bitop3:0x6c
	v_bitop3_b32 v138, v136, v138, 7 bitop3:0x6c
	v_add3_u32 v191, v137, v129, v133
	v_bitop3_b32 v129, v136, v130, 7 bitop3:0x6c
	v_and_b32_e32 v128, 1, v128
	v_lshlrev_b32_e32 v140, 4, v140
	v_lshlrev_b32_e32 v138, 4, v138
	v_lshlrev_b32_e32 v129, 4, v129
	v_lshlrev_b32_e32 v130, 2, v128
	v_and_b32_e32 v131, 7, v158
	s_mov_b64 s[16:17], s[70:71]
	v_add3_u32 v187, v137, v140, v133
	v_add3_u32 v188, v139, v138, v133
	v_add3_u32 v192, v139, v129, v133
	v_bitop3_b32 v132, v130, v158, 7 bitop3:0x78
	v_bitop3_b32 v133, v130, v131, 1 bitop3:0x36
	v_bitop3_b32 v134, v130, v131, 2 bitop3:0x36
	v_bitop3_b32 v130, v130, v131, 3 bitop3:0x36
	v_readlane_b32 s70, v254, 53
	v_lshl_add_u32 v129, v158, 7, s86
	v_lshlrev_b32_e32 v132, 4, v132
	v_lshlrev_b32_e32 v133, 4, v133
	v_lshlrev_b32_e32 v134, 4, v134
	v_lshlrev_b32_e32 v130, 4, v130
	v_readlane_b32 s71, v254, 54
	v_or_b32_e32 v193, 1, v159
	v_or_b32_e32 v194, 2, v159
	v_add_u32_e32 v195, 32, v159
	v_add_u32_e32 v196, 33, v159
	v_add_u32_e32 v197, 34, v159
	v_add_u32_e32 v198, 32, v169
	v_add_u32_e32 v199, 64, v159
	v_add_u32_e32 v200, 0x41, v159
	v_add_u32_e32 v201, 0x42, v159
	v_add_u32_e32 v202, 64, v169
	v_add_u32_e32 v203, 0x60, v159
	v_add_u32_e32 v204, 0x61, v159
	v_add_u32_e32 v205, 0x62, v159
	v_add_u32_e32 v206, 0x60, v169
	v_lshlrev_b32_e32 v146, 6, v128
	v_mov_b32_e32 v147, v157
	s_lshl_b32 s11, s87, 5
	s_lshl_b32 s2, s89, 5
	s_lshl_b32 s13, s87, 2
	s_lshl_b32 s10, s89, 2
	v_add_u32_e32 v207, v129, v132
	v_add_u32_e32 v208, v129, v133
	v_add_u32_e32 v209, v129, v134
	v_add_u32_e32 v210, v129, v130
	s_mov_b32 s37, s87
	s_mov_b32 s64, s5
	s_mov_b32 s57, s12
	v_mov_b32_e32 v148, v164
	s_mov_b64 s[0:1], s[70:71]
	v_mov_b32_e32 v212, v164
	s_waitcnt vmcnt(16)
	s_branch .LBB7_407
.Lf8a_pre_skip_b:
	s_waitcnt vmcnt(0)
	s_branch .LBB7_403

; #define LAS __attribute__((address_space(3)))
; #define LDS_WAIT() asm volatile("s_waitcnt lgkmcnt(0)" ::: "memory")
; __device__ __forceinline__ float cl448(float v) { return fminf(fmaxf(v, -448.0f), 448.0f); }
; __device__ __forceinline__ void f8_pack(const f32x4 (&v)[16], LAS float* scr, int lane) {
;     LAS unsigned* su = (LAS unsigned*)scr; const int nq = lane & 7, kg = lane >> 3;
; #pragma unroll
;     for (int i2 = 0; i2 < 4; ++i2)
; #pragma unroll
;         for (int x = 0; x < 4; ++x) { const int r = 4 * nq + x, chunk = 2 * i2 + (kg >> 2);
;             su[r * 32 + ((chunk ^ (r & 7)) << 2) + (kg & 3)] = pg8::pk4_fp8(cl448(8.0f * v[4 * i2][x]), cl448(8.0f * v[4 * i2 + 1][x]), cl448(8.0f * v[4 * i2 + 2][x]), cl448(8.0f * v[4 * i2 + 3][x])); }
;     LDS_WAIT(); asm volatile("" ::: "memory");
; __device__ __forceinline__ void f8_share(const P& p, LAS unsigned char* ring, int G, int vcu, int wave) {
;     ...
;     while (it < NF8) {
;         { const F8Item cur = ia; f8_pack(va, scr, lane); if (it + 2 * NGW < NF8) { ia = f8_item(p, it + 2 * NGW); f8_load(ia, va, lane); } f8_store(cur, scr, lane); }
.LBB7_407:
	s_waitcnt vmcnt(24)
	v_mul_f32_e32 v128, 0x41000000, v0
	v_med3_f32 v129, v128, s66, v168
	v_mul_f32_e32 v128, 0x41000000, v4
	v_med3_f32 v130, v128, s66, v168
	v_mul_f32_e32 v128, 0x41000000, v8
	v_med3_f32 v131, v128, s66, v168
	v_mul_f32_e32 v128, 0x41000000, v12
	v_med3_f32 v132, v128, s66, v168
	s_add_i32 s53, s37, s89
	v_mov_b32_e32 v133, v128
	v_cvt_pk_fp8_f32 v133, v129, v130
	v_mul_f32_e32 v129, 0x41000000, v1
	v_mul_f32_e32 v130, 0x41000000, v5
	v_med3_f32 v129, v129, s66, v168
	v_cvt_pk_fp8_f32 v133, v131, v132 op_sel:[0,0,1]
	v_med3_f32 v130, v130, s66, v168
	v_mul_f32_e32 v131, 0x41000000, v9
	v_mul_f32_e32 v132, 0x41000000, v13
	ds_write_b32 v170, v133
	v_mov_b32_e32 v133, v128
	v_cvt_pk_fp8_f32 v133, v129, v130
	v_med3_f32 v131, v131, s66, v168
	v_med3_f32 v132, v132, s66, v168
	v_mul_f32_e32 v129, 0x41000000, v2
	v_cvt_pk_fp8_f32 v133, v131, v132 op_sel:[0,0,1]
	v_mul_f32_e32 v130, 0x41000000, v6
	v_med3_f32 v129, v129, s66, v168
	v_med3_f32 v130, v130, s66, v168
	ds_write_b32 v171, v133
	v_mov_b32_e32 v133, v128
	v_cvt_pk_fp8_f32 v133, v129, v130
	v_mul_f32_e32 v131, 0x41000000, v10
	v_mul_f32_e32 v132, 0x41000000, v14
	v_med3_f32 v131, v131, s66, v168
	v_med3_f32 v132, v132, s66, v168
	v_cvt_pk_fp8_f32 v133, v131, v132 op_sel:[0,0,1]
	v_mul_f32_e32 v129, 0x41000000, v3
	v_mul_f32_e32 v130, 0x41000000, v7
	v_med3_f32 v129, v129, s66, v168
	ds_write_b32 v179, v133
	v_med3_f32 v130, v130, s66, v168
	v_mov_b32_e32 v133, v128
	v_cvt_pk_fp8_f32 v133, v129, v130
	v_mul_f32_e32 v131, 0x41000000, v11
	v_mul_f32_e32 v132, 0x41000000, v15
	v_med3_f32 v131, v131, s66, v168
	v_med3_f32 v132, v132, s66, v168
	v_cvt_pk_fp8_f32 v133, v131, v132 op_sel:[0,0,1]
	v_mul_f32_e32 v129, 0x41000000, v16
	v_mul_f32_e32 v130, 0x41000000, v20
	v_med3_f32 v129, v129, s66, v168
	ds_write_b32 v180, v133
	v_med3_f32 v130, v130, s66, v168
	v_mov_b32_e32 v133, v128
	v_cvt_pk_fp8_f32 v133, v129, v130
	v_mul_f32_e32 v131, 0x41000000, v24
	v_mul_f32_e32 v132, 0x41000000, v28
	v_med3_f32 v131, v131, s66, v168
	v_med3_f32 v132, v132, s66, v168
	v_cvt_pk_fp8_f32 v133, v131, v132 op_sel:[0,0,1]
	v_mul_f32_e32 v129, 0x41000000, v17
	v_mul_f32_e32 v130, 0x41000000, v21
	v_med3_f32 v129, v129, s66, v168
	ds_write_b32 v181, v133
	v_med3_f32 v130, v130, s66, v168
	v_mov_b32_e32 v133, v128
	v_cvt_pk_fp8_f32 v133, v129, v130
	v_mul_f32_e32 v131, 0x41000000, v25
	v_mul_f32_e32 v132, 0x41000000, v29
	v_med3_f32 v131, v131, s66, v168
	v_med3_f32 v132, v132, s66, v168
	v_cvt_pk_fp8_f32 v133, v131, v132 op_sel:[0,0,1]
	v_mul_f32_e32 v129, 0x41000000, v18
	v_mul_f32_e32 v130, 0x41000000, v22
	v_med3_f32 v129, v129, s66, v168
	ds_write_b32 v182, v133
	v_med3_f32 v130, v130, s66, v168
	v_mov_b32_e32 v133, v128
	v_cvt_pk_fp8_f32 v133, v129, v130
	v_mul_f32_e32 v131, 0x41000000, v26
	v_mul_f32_e32 v132, 0x41000000, v30
	v_med3_f32 v131, v131, s66, v168
	v_med3_f32 v132, v132, s66, v168
	v_cvt_pk_fp8_f32 v133, v131, v132 op_sel:[0,0,1]
	v_mul_f32_e32 v129, 0x41000000, v19
	v_mul_f32_e32 v130, 0x41000000, v23
	v_med3_f32 v129, v129, s66, v168
	ds_write_b32 v183, v133
	v_med3_f32 v130, v130, s66, v168
	v_mov_b32_e32 v133, v128
	v_cvt_pk_fp8_f32 v133, v129, v130
	v_mul_f32_e32 v131, 0x41000000, v27
	v_mul_f32_e32 v132, 0x41000000, v31
	v_med3_f32 v131, v131, s66, v168
	v_med3_f32 v132, v132, s66, v168
	v_cvt_pk_fp8_f32 v133, v131, v132 op_sel:[0,0,1]
	v_mul_f32_e32 v129, 0x41000000, v32
	v_mul_f32_e32 v130, 0x41000000, v36
	v_med3_f32 v129, v129, s66, v168
	ds_write_b32 v184, v133
	v_med3_f32 v130, v130, s66, v168
	v_mov_b32_e32 v133, v128
	v_cvt_pk_fp8_f32 v133, v129, v130
	v_mul_f32_e32 v131, 0x41000000, v40
	v_mul_f32_e32 v132, 0x41000000, v44
	v_med3_f32 v131, v131, s66, v168
	v_med3_f32 v132, v132, s66, v168
	v_cvt_pk_fp8_f32 v133, v131, v132 op_sel:[0,0,1]
	v_mul_f32_e32 v129, 0x41000000, v33
	v_mul_f32_e32 v130, 0x41000000, v37
	v_med3_f32 v129, v129, s66, v168
	ds_write_b32 v185, v133
	v_med3_f32 v130, v130, s66, v168
	v_mov_b32_e32 v133, v128
	v_cvt_pk_fp8_f32 v133, v129, v130
	v_mul_f32_e32 v131, 0x41000000, v41
	v_mul_f32_e32 v132, 0x41000000, v45
	v_med3_f32 v131, v131, s66, v168
	v_med3_f32 v132, v132, s66, v168
	v_cvt_pk_fp8_f32 v133, v131, v132 op_sel:[0,0,1]
	v_mul_f32_e32 v129, 0x41000000, v34
	v_mul_f32_e32 v130, 0x41000000, v38
	v_med3_f32 v129, v129, s66, v168
	ds_write_b32 v186, v133
	v_med3_f32 v130, v130, s66, v168
	v_mov_b32_e32 v133, v128
	v_cvt_pk_fp8_f32 v133, v129, v130
	v_mul_f32_e32 v131, 0x41000000, v42
	v_mul_f32_e32 v132, 0x41000000, v46
	v_med3_f32 v131, v131, s66, v168
	v_med3_f32 v132, v132, s66, v168
	v_cvt_pk_fp8_f32 v133, v131, v132 op_sel:[0,0,1]
	v_mul_f32_e32 v129, 0x41000000, v35
	v_mul_f32_e32 v130, 0x41000000, v39
	v_med3_f32 v129, v129, s66, v168
	ds_write_b32 v187, v133
	v_med3_f32 v130, v130, s66, v168
	v_mov_b32_e32 v133, v128
	v_cvt_pk_fp8_f32 v133, v129, v130
	v_mul_f32_e32 v131, 0x41000000, v43
	v_mul_f32_e32 v132, 0x41000000, v47
	v_med3_f32 v131, v131, s66, v168
	v_med3_f32 v132, v132, s66, v168
	v_cvt_pk_fp8_f32 v133, v131, v132 op_sel:[0,0,1]
	v_mul_f32_e32 v129, 0x41000000, v48
	v_mul_f32_e32 v130, 0x41000000, v52
	v_med3_f32 v129, v129, s66, v168
	ds_write_b32 v188, v133
	v_med3_f32 v130, v130, s66, v168
	v_mov_b32_e32 v133, v128
	v_cvt_pk_fp8_f32 v133, v129, v130
	v_mul_f32_e32 v131, 0x41000000, v64
	v_mul_f32_e32 v132, 0x41000000, v68
	v_med3_f32 v131, v131, s66, v168
	v_med3_f32 v132, v132, s66, v168
	v_cvt_pk_fp8_f32 v133, v131, v132 op_sel:[0,0,1]
	v_mul_f32_e32 v129, 0x41000000, v49
	v_mul_f32_e32 v130, 0x41000000, v53
	v_med3_f32 v129, v129, s66, v168
	ds_write_b32 v189, v133
	v_med3_f32 v130, v130, s66, v168
	v_mov_b32_e32 v133, v128
	v_cvt_pk_fp8_f32 v133, v129, v130
	v_mul_f32_e32 v131, 0x41000000, v65
	v_mul_f32_e32 v132, 0x41000000, v69
	v_med3_f32 v131, v131, s66, v168
	v_med3_f32 v132, v132, s66, v168
	v_cvt_pk_fp8_f32 v133, v131, v132 op_sel:[0,0,1]
	v_mul_f32_e32 v129, 0x41000000, v50
	v_mul_f32_e32 v130, 0x41000000, v54
	v_med3_f32 v129, v129, s66, v168
	ds_write_b32 v190, v133
	v_med3_f32 v130, v130, s66, v168
	v_mov_b32_e32 v133, v128
	v_cvt_pk_fp8_f32 v133, v129, v130
	v_mul_f32_e32 v129, 0x41000000, v51
	v_mul_f32_e32 v130, 0x41000000, v55
	v_med3_f32 v129, v129, s66, v168
	v_med3_f32 v130, v130, s66, v168
	v_mul_f32_e32 v131, 0x41000000, v66
	v_mul_f32_e32 v132, 0x41000000, v70
	v_cvt_pk_fp8_f32 v128, v129, v130
	v_med3_f32 v131, v131, s66, v168
	v_med3_f32 v132, v132, s66, v168
	v_cvt_pk_fp8_f32 v133, v131, v132 op_sel:[0,0,1]
	v_mul_f32_e32 v131, 0x41000000, v67
	v_mul_f32_e32 v132, 0x41000000, v71
	v_med3_f32 v131, v131, s66, v168
	v_med3_f32 v132, v132, s66, v168
	v_cvt_pk_fp8_f32 v128, v131, v132 op_sel:[0,0,1]
	ds_write_b32 v191, v133
	s_cmpk_gt_i32 s53, 0x5fff
	s_cselect_b64 s[60:61], -1, 0
	ds_write_b32 v192, v128
	s_waitcnt lgkmcnt(0)
	s_and_b64 vcc, exec, s[60:61]
	s_mov_b32 s94, s64
	s_mov_b32 s62, s57
	s_cbranch_vccnz .Lf8a_skip_a
; __device__ __forceinline__ F8Item f8_item(const P& p, int r) {
;     constexpr int I_W1 = 8 * 64, I_W2 = 8 * 32; F8Item it;
;     if (r < NE * I_W1) { const int e = r / I_W1, q = r % I_W1; it.W = p.w1 + (size_t)e * DM * 2048; it.WT = p.ws + WS_W1T + (size_t)e * 2048 * DM; it.N = 2048; it.k0 = 128 * (q / 64); it.n0 = 32 * (q % 64); it.map = 1; }
;     else { r -= NE * I_W1; const int e = r / I_W2, q = r % I_W2; it.W = p.w2 + (size_t)e * DM * DM; it.WT = p.ws + WS_W2T + (size_t)e * DM * DM; it.N = DM; it.k0 = 128 * (q / 32); it.n0 = 32 * (q % 32); it.map = 0; }
;     return it;
; }
; __device__ __forceinline__ void f8_share(const P& p, LAS unsigned char* ring, int G, int vcu, int wave) {
;     ...
;         { const F8Item cur = ia; f8_pack(va, scr, lane); if (it + 2 * NGW < NF8) { ia = f8_item(p, it + 2 * NGW); f8_load(ia, va, lane); } f8_store(cur, scr, lane); }
	s_cmpk_gt_i32 s53, 0x3fff
	s_mov_b64 s[74:75], -1
	s_cbranch_scc0 .LBB7_410
	s_add_i32 s0, s53, 0xffffc000
	s_lshr_b32 s8, s0, 8
	s_lshl_b64 s[0:1], s[8:9], 20
	s_lshl_b64 s[62:63], s[8:9], 22
	s_add_u32 s72, s24, s62
	s_addc_u32 s73, s25, s63
	s_add_u32 s0, s68, s0
	s_addc_u32 s1, s69, s1
	s_add_i32 s8, s10, s13
	s_and_b32 s94, s8, 0x380
	s_add_i32 s8, s2, s11
	s_and_b32 s62, s8, 0x3e0
	s_mov_b64 s[74:75], 0

; __device__ __forceinline__ void f8_share(const P& p, LAS unsigned char* ring, int G, int vcu, int wave) {
;     ...
;         { const F8Item cur = ia; f8_pack(va, scr, lane); if (it + 2 * NGW < NF8) { ia = f8_item(p, it + 2 * NGW); f8_load(ia, va, lane); } f8_store(cur, scr, lane); }
.Lf8a_skip_a:
	s_waitcnt vmcnt(4)
	s_branch .LBB7_414

; #define LAS __attribute__((address_space(3)))
; #define LDS_WAIT() asm volatile("s_waitcnt lgkmcnt(0)" ::: "memory")
; __device__ __forceinline__ int rmap_w2(int c) { const int cc = c & 255; return (c & ~255) + 128 * ((cc >> 3) & 1) + 32 * (cc >> 6) + 8 * ((cc >> 4) & 3) + (cc & 7); }
; __device__ __forceinline__ float cl448(float v) { return fminf(fmaxf(v, -448.0f), 448.0f); }
; __device__ __forceinline__ void f8_pack(const f32x4 (&v)[16], LAS float* scr, int lane) {
;     LAS unsigned* su = (LAS unsigned*)scr; const int nq = lane & 7, kg = lane >> 3;
; #pragma unroll
;     for (int i2 = 0; i2 < 4; ++i2)
; #pragma unroll
;         for (int x = 0; x < 4; ++x) { const int r = 4 * nq + x, chunk = 2 * i2 + (kg >> 2);
;             su[r * 32 + ((chunk ^ (r & 7)) << 2) + (kg & 3)] = pg8::pk4_fp8(cl448(8.0f * v[4 * i2][x]), cl448(8.0f * v[4 * i2 + 1][x]), cl448(8.0f * v[4 * i2 + 2][x]), cl448(8.0f * v[4 * i2 + 3][x])); }
;     LDS_WAIT(); asm volatile("" ::: "memory");
; }
; __device__ __forceinline__ void f8_store(const F8Item& it, LAS float* scr, int lane) {
;     const LAS unsigned* su = (const LAS unsigned*)scr; const int n = lane >> 1, half = lane & 1;
;     u32x4 o[4];
; #pragma unroll
;     for (int q = 0; q < 4; ++q) o[q] = *(const LAS u32x4*)(su + n * 32 + (((4 * half + q) ^ (n & 7)) << 2));
;     const int src = it.n0 + n; const int row = it.map ? rmap_w1(src) : rmap_w2(src); unsigned char* dst = it.WT + (size_t)row * DM + it.k0 + 64 * half;
; #pragma unroll
;     for (int q = 0; q < 4; ++q) *(u32x4*)(dst + 16 * q) = o[q];
;     LDS_WAIT(); asm volatile("" ::: "memory");
; }
; __device__ __forceinline__ void f8_share(const P& p, LAS unsigned char* ring, int G, int vcu, int wave) {
;     ...
;         if (it + NGW >= NF8) break;
;         { const F8Item cur = ib; f8_pack(vb, scr, lane); if (it + 3 * NGW < NF8) { ib = f8_item(p, it + 3 * NGW); f8_load(ib, vb, lane); } f8_store(cur, scr, lane); }
.LBB7_417:
	v_ashrrev_i32_e32 v149, 31, v148
	v_lshlrev_b64 v[148:149], 10, v[148:149]
	v_lshl_add_u64 v[148:149], s[70:71], 0, v[148:149]
	s_ashr_i32 s65, s64, 31
	v_lshl_add_u64 v[148:149], v[148:149], 0, s[64:65]
	v_lshl_add_u64 v[148:149], v[148:149], 0, v[146:147]
	s_waitcnt lgkmcnt(3)
	global_store_dwordx4 v[148:149], v[128:131], off
	s_waitcnt lgkmcnt(2)
	global_store_dwordx4 v[148:149], v[132:135], off offset:16
	s_waitcnt lgkmcnt(1)
	global_store_dwordx4 v[148:149], v[136:139], off offset:32
	s_waitcnt lgkmcnt(0)
	global_store_dwordx4 v[148:149], v[140:143], off offset:48
	s_waitcnt lgkmcnt(0)
	s_add_i32 s8, s88, s37
	s_cmpk_gt_i32 s8, 0x5fff
	s_cbranch_scc1 .LBB7_405
	s_waitcnt vmcnt(20)
	v_mul_f32_e32 v128, 0x41000000, v56
	v_med3_f32 v129, v128, s66, v168
	v_mul_f32_e32 v128, 0x41000000, v60
	v_med3_f32 v130, v128, s66, v168
	v_mul_f32_e32 v128, 0x41000000, v72
	v_med3_f32 v131, v128, s66, v168
	v_mul_f32_e32 v128, 0x41000000, v76
	v_med3_f32 v132, v128, s66, v168
	s_mul_i32 s8, s3, 24
	v_mov_b32_e32 v133, v128
	v_cvt_pk_fp8_f32 v133, v129, v130
	v_mul_f32_e32 v129, 0x41000000, v57
	v_mul_f32_e32 v130, 0x41000000, v61
	v_med3_f32 v129, v129, s66, v168
	v_cvt_pk_fp8_f32 v133, v131, v132 op_sel:[0,0,1]
	v_med3_f32 v130, v130, s66, v168
	v_mul_f32_e32 v131, 0x41000000, v73
	v_mul_f32_e32 v132, 0x41000000, v77
	ds_write_b32 v170, v133
	v_mov_b32_e32 v133, v128
	v_cvt_pk_fp8_f32 v133, v129, v130
	v_med3_f32 v131, v131, s66, v168
	v_med3_f32 v132, v132, s66, v168
	v_mul_f32_e32 v129, 0x41000000, v58
	v_cvt_pk_fp8_f32 v133, v131, v132 op_sel:[0,0,1]
	v_mul_f32_e32 v130, 0x41000000, v62
	v_med3_f32 v129, v129, s66, v168
	v_med3_f32 v130, v130, s66, v168
	ds_write_b32 v171, v133
	v_mov_b32_e32 v133, v128
	v_cvt_pk_fp8_f32 v133, v129, v130
	v_mul_f32_e32 v131, 0x41000000, v74
	v_mul_f32_e32 v132, 0x41000000, v78
	v_med3_f32 v131, v131, s66, v168
	v_med3_f32 v132, v132, s66, v168
	v_cvt_pk_fp8_f32 v133, v131, v132 op_sel:[0,0,1]
	v_mul_f32_e32 v129, 0x41000000, v59
	v_mul_f32_e32 v130, 0x41000000, v63
	v_med3_f32 v129, v129, s66, v168
	ds_write_b32 v179, v133
	v_med3_f32 v130, v130, s66, v168
	v_mov_b32_e32 v133, v128
	v_cvt_pk_fp8_f32 v133, v129, v130
	v_mul_f32_e32 v131, 0x41000000, v75
	v_mul_f32_e32 v132, 0x41000000, v79
	v_med3_f32 v131, v131, s66, v168
	v_med3_f32 v132, v132, s66, v168
	v_cvt_pk_fp8_f32 v133, v131, v132 op_sel:[0,0,1]
	v_mul_f32_e32 v129, 0x41000000, v80
	v_mul_f32_e32 v130, 0x41000000, v84
	v_med3_f32 v129, v129, s66, v168
	ds_write_b32 v180, v133
	v_med3_f32 v130, v130, s66, v168
	v_mov_b32_e32 v133, v128
	v_cvt_pk_fp8_f32 v133, v129, v130
	v_mul_f32_e32 v131, 0x41000000, v88
	v_mul_f32_e32 v132, 0x41000000, v92
	v_med3_f32 v131, v131, s66, v168
	v_med3_f32 v132, v132, s66, v168
	v_cvt_pk_fp8_f32 v133, v131, v132 op_sel:[0,0,1]
	v_mul_f32_e32 v129, 0x41000000, v81
	v_mul_f32_e32 v130, 0x41000000, v85
	v_med3_f32 v129, v129, s66, v168
	ds_write_b32 v181, v133
	v_med3_f32 v130, v130, s66, v168
	v_mov_b32_e32 v133, v128
	v_cvt_pk_fp8_f32 v133, v129, v130
	v_mul_f32_e32 v131, 0x41000000, v89
	v_mul_f32_e32 v132, 0x41000000, v93
	v_med3_f32 v131, v131, s66, v168
	v_med3_f32 v132, v132, s66, v168
	v_cvt_pk_fp8_f32 v133, v131, v132 op_sel:[0,0,1]
	v_mul_f32_e32 v129, 0x41000000, v82
	v_mul_f32_e32 v130, 0x41000000, v86
	v_med3_f32 v129, v129, s66, v168
	ds_write_b32 v182, v133
	v_med3_f32 v130, v130, s66, v168
	v_mov_b32_e32 v133, v128
	v_cvt_pk_fp8_f32 v133, v129, v130
	v_mul_f32_e32 v131, 0x41000000, v90
	v_mul_f32_e32 v132, 0x41000000, v94
	v_med3_f32 v131, v131, s66, v168
	v_med3_f32 v132, v132, s66, v168
	v_cvt_pk_fp8_f32 v133, v131, v132 op_sel:[0,0,1]
	v_mul_f32_e32 v129, 0x41000000, v83
	v_mul_f32_e32 v130, 0x41000000, v87
	v_med3_f32 v129, v129, s66, v168
	ds_write_b32 v183, v133
	v_med3_f32 v130, v130, s66, v168
	v_mov_b32_e32 v133, v128
	v_cvt_pk_fp8_f32 v133, v129, v130
	v_mul_f32_e32 v131, 0x41000000, v91
	v_mul_f32_e32 v132, 0x41000000, v95
	v_med3_f32 v131, v131, s66, v168
	v_med3_f32 v132, v132, s66, v168
	v_cvt_pk_fp8_f32 v133, v131, v132 op_sel:[0,0,1]
; #define LAS __attribute__((address_space(3)))
; #define LDS_WAIT() asm volatile("s_waitcnt lgkmcnt(0)" ::: "memory")
; __device__ __forceinline__ float cl448(float v) { return fminf(fmaxf(v, -448.0f), 448.0f); }
; __device__ __forceinline__ F8Item f8_item(const P& p, int r) {
;     constexpr int I_W1 = 8 * 64, I_W2 = 8 * 32; F8Item it;
;     if (r < NE * I_W1) { const int e = r / I_W1, q = r % I_W1; it.W = p.w1 + (size_t)e * DM * 2048; it.WT = p.ws + WS_W1T + (size_t)e * 2048 * DM; it.N = 2048; it.k0 = 128 * (q / 64); it.n0 = 32 * (q % 64); it.map = 1; }
;     else { r -= NE * I_W1; const int e = r / I_W2, q = r % I_W2; it.W = p.w2 + (size_t)e * DM * DM; it.WT = p.ws + WS_W2T + (size_t)e * DM * DM; it.N = DM; it.k0 = 128 * (q / 32); it.n0 = 32 * (q % 32); it.map = 0; }
;     return it;
; }
; __device__ __forceinline__ void f8_load(const F8Item& it, f32x4 (&v)[16], int lane) {
; #pragma unroll
;     for (int i = 0; i < 16; ++i) v[i] = *(const f32x4*)(it.W + (size_t)(it.k0 + 32 * (i >> 2) + 4 * (lane >> 3) + (i & 3)) * it.N + it.n0 + 4 * (lane & 7));
; }
; __device__ __forceinline__ void f8_pack(const f32x4 (&v)[16], LAS float* scr, int lane) {
;     LAS unsigned* su = (LAS unsigned*)scr; const int nq = lane & 7, kg = lane >> 3;
; #pragma unroll
;     for (int i2 = 0; i2 < 4; ++i2)
; #pragma unroll
;         for (int x = 0; x < 4; ++x) { const int r = 4 * nq + x, chunk = 2 * i2 + (kg >> 2);
;             su[r * 32 + ((chunk ^ (r & 7)) << 2) + (kg & 3)] = pg8::pk4_fp8(cl448(8.0f * v[4 * i2][x]), cl448(8.0f * v[4 * i2 + 1][x]), cl448(8.0f * v[4 * i2 + 2][x]), cl448(8.0f * v[4 * i2 + 3][x])); }
;     LDS_WAIT(); asm volatile("" ::: "memory");
; __device__ __forceinline__ void f8_share(const P& p, LAS unsigned char* ring, int G, int vcu, int wave) {
;     ...
;         { const F8Item cur = ib; f8_pack(vb, scr, lane); if (it + 3 * NGW < NF8) { ib = f8_item(p, it + 3 * NGW); f8_load(ib, vb, lane); } f8_store(cur, scr, lane); }
	v_mul_f32_e32 v129, 0x41000000, v96
	v_mul_f32_e32 v130, 0x41000000, v100
	v_med3_f32 v129, v129, s66, v168
	ds_write_b32 v184, v133
	v_med3_f32 v130, v130, s66, v168
	v_mov_b32_e32 v133, v128
	v_cvt_pk_fp8_f32 v133, v129, v130
	v_mul_f32_e32 v131, 0x41000000, v104
	v_mul_f32_e32 v132, 0x41000000, v108
	v_med3_f32 v131, v131, s66, v168
	v_med3_f32 v132, v132, s66, v168
	v_cvt_pk_fp8_f32 v133, v131, v132 op_sel:[0,0,1]
	v_mul_f32_e32 v129, 0x41000000, v97
	v_mul_f32_e32 v130, 0x41000000, v101
	v_med3_f32 v129, v129, s66, v168
	ds_write_b32 v185, v133
	v_med3_f32 v130, v130, s66, v168
	v_mov_b32_e32 v133, v128
	v_cvt_pk_fp8_f32 v133, v129, v130
	v_mul_f32_e32 v131, 0x41000000, v105
	v_mul_f32_e32 v132, 0x41000000, v109
	v_med3_f32 v131, v131, s66, v168
	v_med3_f32 v132, v132, s66, v168
	v_cvt_pk_fp8_f32 v133, v131, v132 op_sel:[0,0,1]
	v_mul_f32_e32 v129, 0x41000000, v98
	v_mul_f32_e32 v130, 0x41000000, v102
	v_med3_f32 v129, v129, s66, v168
	ds_write_b32 v186, v133
	v_med3_f32 v130, v130, s66, v168
	v_mov_b32_e32 v133, v128
	v_cvt_pk_fp8_f32 v133, v129, v130
	v_mul_f32_e32 v131, 0x41000000, v106
	v_mul_f32_e32 v132, 0x41000000, v110
	v_med3_f32 v131, v131, s66, v168
	v_med3_f32 v132, v132, s66, v168
	v_cvt_pk_fp8_f32 v133, v131, v132 op_sel:[0,0,1]
	v_mul_f32_e32 v129, 0x41000000, v99
	v_mul_f32_e32 v130, 0x41000000, v103
	v_med3_f32 v129, v129, s66, v168
	ds_write_b32 v187, v133
	v_med3_f32 v130, v130, s66, v168
	v_mov_b32_e32 v133, v128
	v_cvt_pk_fp8_f32 v133, v129, v130
	v_mul_f32_e32 v131, 0x41000000, v107
	v_mul_f32_e32 v132, 0x41000000, v111
	v_med3_f32 v131, v131, s66, v168
	v_med3_f32 v132, v132, s66, v168
	v_cvt_pk_fp8_f32 v133, v131, v132 op_sel:[0,0,1]
	v_mul_f32_e32 v129, 0x41000000, v112
	v_mul_f32_e32 v130, 0x41000000, v116
	v_med3_f32 v129, v129, s66, v168
	ds_write_b32 v188, v133
	v_med3_f32 v130, v130, s66, v168
	v_mov_b32_e32 v133, v128
	v_cvt_pk_fp8_f32 v133, v129, v130
	v_mul_f32_e32 v131, 0x41000000, v120
	v_mul_f32_e32 v132, 0x41000000, v124
	v_med3_f32 v131, v131, s66, v168
	v_med3_f32 v132, v132, s66, v168
	v_cvt_pk_fp8_f32 v133, v131, v132 op_sel:[0,0,1]
	v_mul_f32_e32 v129, 0x41000000, v113
	v_mul_f32_e32 v130, 0x41000000, v117
	v_med3_f32 v129, v129, s66, v168
	ds_write_b32 v189, v133
	v_med3_f32 v130, v130, s66, v168
	v_mov_b32_e32 v133, v128
	v_cvt_pk_fp8_f32 v133, v129, v130
	v_mul_f32_e32 v131, 0x41000000, v121
	v_mul_f32_e32 v132, 0x41000000, v125
	v_med3_f32 v131, v131, s66, v168
	v_med3_f32 v132, v132, s66, v168
	v_cvt_pk_fp8_f32 v133, v131, v132 op_sel:[0,0,1]
	v_mul_f32_e32 v129, 0x41000000, v114
	v_mul_f32_e32 v130, 0x41000000, v118
	v_med3_f32 v129, v129, s66, v168
	ds_write_b32 v190, v133
	v_med3_f32 v130, v130, s66, v168
	v_mov_b32_e32 v133, v128
	v_cvt_pk_fp8_f32 v133, v129, v130
	v_mul_f32_e32 v129, 0x41000000, v115
	v_mul_f32_e32 v130, 0x41000000, v119
	v_med3_f32 v129, v129, s66, v168
	v_med3_f32 v130, v130, s66, v168
	v_mul_f32_e32 v131, 0x41000000, v122
	v_mul_f32_e32 v132, 0x41000000, v126
	v_cvt_pk_fp8_f32 v128, v129, v130
	v_med3_f32 v131, v131, s66, v168
	v_med3_f32 v132, v132, s66, v168
	v_cvt_pk_fp8_f32 v133, v131, v132 op_sel:[0,0,1]
	v_mul_f32_e32 v131, 0x41000000, v123
	v_mul_f32_e32 v132, 0x41000000, v127
	v_med3_f32 v131, v131, s66, v168
	v_med3_f32 v132, v132, s66, v168
	v_cvt_pk_fp8_f32 v128, v131, v132 op_sel:[0,0,1]
	ds_write_b32 v191, v133
	s_add_i32 s37, s8, s37
	s_cmpk_gt_i32 s37, 0x5fff
	ds_write_b32 v192, v128
	s_waitcnt lgkmcnt(0)
	s_mov_b64 s[64:65], s[58:59]
	s_mov_b32 s8, s56
	s_mov_b32 s70, s36
	v_mov_b32_e32 v156, v211
	s_cbranch_scc1 .Lf8a_skip_b
	s_cmpk_gt_i32 s37, 0x3fff
	s_mov_b64 s[74:75], -1
	s_cbranch_scc0 .LBB7_421
	s_add_i32 s8, s37, 0xffffc000
	s_lshr_b32 s8, s8, 8
	s_lshl_b64 s[64:65], s[8:9], 20
	s_lshl_b64 s[70:71], s[8:9], 22
	s_add_u32 s72, s24, s70
	s_addc_u32 s73, s25, s71
	s_add_u32 s64, s68, s64
	s_mul_i32 s8, s3, 0x60
	s_mul_i32 s57, s3, 0x300
	s_addc_u32 s65, s69, s65
	s_add_i32 s8, s8, s13
	s_add_i32 s57, s57, s11
	s_and_b32 s8, s8, 0x380
	s_and_b32 s70, s57, 0x3e0
	s_mov_b64 s[74:75], 0

; __device__ __forceinline__ void f8_load(const F8Item& it, f32x4 (&v)[16], int lane) {
; #pragma unroll
;     for (int i = 0; i < 16; ++i) v[i] = *(const f32x4*)(it.W + (size_t)(it.k0 + 32 * (i >> 2) + 4 * (lane >> 3) + (i & 3)) * it.N + it.n0 + 4 * (lane & 7));
; }
; __device__ __forceinline__ void f8_share(const P& p, LAS unsigned char* ring, int G, int vcu, int wave) {
;     ...
;     if (it + NGW < NF8) { ib = f8_item(p, it + NGW); f8_load(ib, vb, lane); }
;     while (it < NF8) {
;         { const F8Item cur = ia; f8_pack(va, scr, lane); if (it + 2 * NGW < NF8) { ia = f8_item(p, it + 2 * NGW); f8_load(ia, va, lane); } f8_store(cur, scr, lane); }
;         if (it + NGW >= NF8) break;
;         { const F8Item cur = ib; f8_pack(vb, scr, lane); if (it + 3 * NGW < NF8) { ib = f8_item(p, it + 3 * NGW); f8_load(ib, vb, lane); } f8_store(cur, scr, lane); }
.LBB7_454:
	v_readlane_b32 s8, v254, 59
	v_readlane_b32 s9, v254, 60
	s_andn2_b64 vcc, exec, s[8:9]
	v_readlane_b32 s8, v254, 53
	v_readlane_b32 s48, v254, 56
	v_mov_b32_e32 v210, v152
	s_mov_b32 s37, s8
	s_mov_b32 s46, s76
	v_readlane_b32 s49, v254, 57
	v_readlane_b32 s9, v254, 54
	s_cbranch_vccnz .Lf8b_pre_skip_b
	v_readlane_b32 s6, v255, 6
	v_readlane_b32 s8, v255, 9
	v_readlane_b32 s48, v255, 7
	v_add_u32_e32 v120, s6, v174
	v_add_u32_e32 v122, s6, v175
	v_ashrrev_i32_e32 v121, 31, v120
	v_ashrrev_i32_e32 v123, 31, v122
	v_lshlrev_b64 v[56:57], s93, v[120:121]
	v_or_b32_e32 v58, 1, v120
	s_waitcnt vmcnt(16)
	v_or_b32_e32 v72, 2, v120
	v_lshlrev_b64 v[74:75], s93, v[122:123]
	v_add_u32_e32 v80, 32, v120
	v_add_u32_e32 v82, 33, v120
	v_add_u32_e32 v88, 34, v120
	v_add_u32_e32 v90, 32, v122
	v_add_u32_e32 v96, 64, v120
	v_add_u32_e32 v98, 0x41, v120
	v_add_u32_e32 v104, 0x42, v120
	v_add_u32_e32 v106, 64, v122
	v_add_u32_e32 v112, 0x60, v120
	v_add_u32_e32 v114, 0x61, v120
	v_add_u32_e32 v120, 0x62, v120
	v_add_u32_e32 v122, 0x60, v122
	v_ashrrev_i32_e32 v59, 31, v58
	v_ashrrev_i32_e32 v73, 31, v72
	v_ashrrev_i32_e32 v81, 31, v80
	v_ashrrev_i32_e32 v83, 31, v82
	v_ashrrev_i32_e32 v89, 31, v88
	v_ashrrev_i32_e32 v91, 31, v90
	v_ashrrev_i32_e32 v97, 31, v96
	v_ashrrev_i32_e32 v99, 31, v98
	v_ashrrev_i32_e32 v105, 31, v104
	v_ashrrev_i32_e32 v107, 31, v106
	v_ashrrev_i32_e32 v113, 31, v112
	v_ashrrev_i32_e32 v115, 31, v114
	v_ashrrev_i32_e32 v121, 31, v120
	v_ashrrev_i32_e32 v123, 31, v122
	v_lshlrev_b64 v[58:59], s93, v[58:59]
	v_lshlrev_b64 v[72:73], s93, v[72:73]
	v_lshlrev_b64 v[80:81], s93, v[80:81]
	v_lshlrev_b64 v[82:83], s93, v[82:83]
	v_lshlrev_b64 v[88:89], s93, v[88:89]
	v_lshlrev_b64 v[90:91], s93, v[90:91]
	v_lshlrev_b64 v[96:97], s93, v[96:97]
	v_lshlrev_b64 v[98:99], s93, v[98:99]
	v_lshlrev_b64 v[104:105], s93, v[104:105]
	v_lshlrev_b64 v[106:107], s93, v[106:107]
	v_lshlrev_b64 v[112:113], s93, v[112:113]
	v_lshlrev_b64 v[114:115], s93, v[114:115]
	v_lshlrev_b64 v[120:121], s93, v[120:121]
	v_lshlrev_b64 v[122:123], s93, v[122:123]
	v_lshl_add_u64 v[56:57], v[56:57], 2, s[42:43]
	v_lshl_add_u64 v[58:59], v[58:59], 2, s[42:43]
	v_lshl_add_u64 v[72:73], v[72:73], 2, s[42:43]
	v_lshl_add_u64 v[74:75], v[74:75], 2, s[42:43]
	v_lshl_add_u64 v[80:81], v[80:81], 2, s[42:43]
	v_lshl_add_u64 v[82:83], v[82:83], 2, s[42:43]
	v_lshl_add_u64 v[88:89], v[88:89], 2, s[42:43]
	v_lshl_add_u64 v[90:91], v[90:91], 2, s[42:43]
	v_lshl_add_u64 v[96:97], v[96:97], 2, s[42:43]
	v_lshl_add_u64 v[98:99], v[98:99], 2, s[42:43]
	v_lshl_add_u64 v[104:105], v[104:105], 2, s[42:43]
	v_lshl_add_u64 v[106:107], v[106:107], 2, s[42:43]
	v_lshl_add_u64 v[112:113], v[112:113], 2, s[42:43]
	v_lshl_add_u64 v[114:115], v[114:115], 2, s[42:43]
	v_lshl_add_u64 v[120:121], v[120:121], 2, s[42:43]
	v_lshl_add_u64 v[122:123], v[122:123], 2, s[42:43]
	v_lshl_add_u64 v[56:57], v[56:57], 0, v[144:145]
	v_lshl_add_u64 v[60:61], v[58:59], 0, v[144:145]
	v_lshl_add_u64 v[72:73], v[72:73], 0, v[144:145]
	v_lshl_add_u64 v[76:77], v[74:75], 0, v[144:145]
	v_lshl_add_u64 v[80:81], v[80:81], 0, v[144:145]
	v_lshl_add_u64 v[84:85], v[82:83], 0, v[144:145]
	v_lshl_add_u64 v[88:89], v[88:89], 0, v[144:145]
	v_lshl_add_u64 v[92:93], v[90:91], 0, v[144:145]
	v_lshl_add_u64 v[96:97], v[96:97], 0, v[144:145]
	v_lshl_add_u64 v[100:101], v[98:99], 0, v[144:145]
	v_lshl_add_u64 v[104:105], v[104:105], 0, v[144:145]
	v_lshl_add_u64 v[108:109], v[106:107], 0, v[144:145]
	v_lshl_add_u64 v[112:113], v[112:113], 0, v[144:145]
	v_lshl_add_u64 v[116:117], v[114:115], 0, v[144:145]
	v_lshl_add_u64 v[120:121], v[120:121], 0, v[144:145]
	v_lshl_add_u64 v[124:125], v[122:123], 0, v[144:145]
	global_load_dwordx4 v[56:59], v[56:57], off
	s_nop 0
	global_load_dwordx4 v[60:63], v[60:61], off
	s_nop 0
	global_load_dwordx4 v[72:75], v[72:73], off
	s_nop 0
	global_load_dwordx4 v[76:79], v[76:77], off
	s_nop 0
	global_load_dwordx4 v[80:83], v[80:81], off
	s_nop 0
	global_load_dwordx4 v[84:87], v[84:85], off
	s_nop 0
	global_load_dwordx4 v[88:91], v[88:89], off
	s_nop 0
	global_load_dwordx4 v[92:95], v[92:93], off
	s_nop 0
	global_load_dwordx4 v[96:99], v[96:97], off
	s_nop 0
	global_load_dwordx4 v[100:103], v[100:101], off
	s_nop 0
	global_load_dwordx4 v[104:107], v[104:105], off
	s_nop 0
	global_load_dwordx4 v[108:111], v[108:109], off
	s_nop 0
	global_load_dwordx4 v[112:115], v[112:113], off
	s_nop 0
	global_load_dwordx4 v[116:119], v[116:117], off
	s_nop 0
	global_load_dwordx4 v[120:123], v[120:121], off
	s_nop 0
	global_load_dwordx4 v[124:127], v[124:125], off
	v_mov_b32_e32 v210, v153
	s_mov_b32 s37, s8
	s_mov_b32 s46, s6
	v_readlane_b32 s49, v255, 8
	v_readlane_b32 s9, v255, 10
; #define LAS __attribute__((address_space(3)))
; #define LDS_WAIT() asm volatile("s_waitcnt lgkmcnt(0)" ::: "memory")
; __device__ __forceinline__ int rmap_w2(int c) { const int cc = c & 255; return (c & ~255) + 128 * ((cc >> 3) & 1) + 32 * (cc >> 6) + 8 * ((cc >> 4) & 3) + (cc & 7); }
; __device__ __forceinline__ float cl448(float v) { return fminf(fmaxf(v, -448.0f), 448.0f); }
; __device__ __forceinline__ void f8_pack(const f32x4 (&v)[16], LAS float* scr, int lane) {
;     LAS unsigned* su = (LAS unsigned*)scr; const int nq = lane & 7, kg = lane >> 3;
; #pragma unroll
;     for (int i2 = 0; i2 < 4; ++i2)
; #pragma unroll
;         for (int x = 0; x < 4; ++x) { const int r = 4 * nq + x, chunk = 2 * i2 + (kg >> 2);
;             su[r * 32 + ((chunk ^ (r & 7)) << 2) + (kg & 3)] = pg8::pk4_fp8(cl448(8.0f * v[4 * i2][x]), cl448(8.0f * v[4 * i2 + 1][x]), cl448(8.0f * v[4 * i2 + 2][x]), cl448(8.0f * v[4 * i2 + 3][x])); }
;     LDS_WAIT(); asm volatile("" ::: "memory");
; }
; __device__ __forceinline__ void f8_store(const F8Item& it, LAS float* scr, int lane) {
;     const LAS unsigned* su = (const LAS unsigned*)scr; const int n = lane >> 1, half = lane & 1;
;     u32x4 o[4];
; #pragma unroll
;     for (int q = 0; q < 4; ++q) o[q] = *(const LAS u32x4*)(su + n * 32 + (((4 * half + q) ^ (n & 7)) << 2));
;     const int src = it.n0 + n; const int row = it.map ? rmap_w1(src) : rmap_w2(src); unsigned char* dst = it.WT + (size_t)row * DM + it.k0 + 64 * half;
.LBB7_456:
	s_and_b64 vcc, exec, s[0:1]
	s_cbranch_vccnz .LBB7_484
	v_lshlrev_b32_e32 v129, 2, v128
	v_ashrrev_i32_e32 v130, 5, v128
	v_and_b32_e32 v146, 28, v129
	v_bitop3_b32 v131, v129, v130, 4 bitop3:0x6c
	v_lshrrev_b32_e32 v133, 1, v128
	v_lshl_add_u32 v132, v146, 7, s4
	v_lshlrev_b32_e32 v131, 4, v131
	v_and_b32_e32 v133, 12, v133
	v_add3_u32 v176, v132, v131, v133
	v_or_b32_e32 v131, 1, v146
	v_bitop3_b32 v134, v131, v130, 5 bitop3:0x6c
	v_lshl_add_u32 v135, v131, 7, s4
	v_lshlrev_b32_e32 v134, 4, v134
	v_add3_u32 v177, v135, v134, v133
	v_or_b32_e32 v134, 2, v146
	v_bitop3_b32 v136, v134, v130, 6 bitop3:0x6c
	v_lshl_add_u32 v137, v134, 7, s4
	v_lshlrev_b32_e32 v136, 4, v136
	v_add3_u32 v178, v137, v136, v133
	v_or_b32_e32 v136, 3, v146
	v_bitop3_b32 v138, v136, v130, 7 bitop3:0x6c
	v_lshl_add_u32 v139, v136, 7, s4
	v_lshlrev_b32_e32 v138, 4, v138
	v_add3_u32 v179, v139, v138, v133
	v_add_u32_e32 v138, 2, v130
	v_bitop3_b32 v140, v129, v138, 4 bitop3:0x6c
	v_lshlrev_b32_e32 v140, 4, v140
	v_add3_u32 v180, v132, v140, v133
	v_bitop3_b32 v140, v131, v138, 5 bitop3:0x6c
	v_lshlrev_b32_e32 v140, 4, v140
	v_add3_u32 v181, v135, v140, v133
	v_bitop3_b32 v140, v134, v138, 6 bitop3:0x6c
	v_bitop3_b32 v138, v136, v138, 7 bitop3:0x6c
	v_lshlrev_b32_e32 v138, 4, v138
	v_lshlrev_b32_e32 v140, 4, v140
	v_add3_u32 v183, v139, v138, v133
	v_add_u32_e32 v138, 4, v130
	v_add_u32_e32 v130, 6, v130
	v_add3_u32 v182, v137, v140, v133
	v_bitop3_b32 v140, v129, v138, 4 bitop3:0x6c
	v_bitop3_b32 v129, v129, v130, 4 bitop3:0x6c
	v_lshlrev_b32_e32 v129, 4, v129
	v_add3_u32 v188, v132, v129, v133
	v_bitop3_b32 v129, v131, v130, 5 bitop3:0x6c
	v_lshlrev_b32_e32 v140, 4, v140
	v_lshlrev_b32_e32 v129, 4, v129
	v_add3_u32 v184, v132, v140, v133
	v_bitop3_b32 v140, v131, v138, 5 bitop3:0x6c
	v_add3_u32 v189, v135, v129, v133
	v_bitop3_b32 v129, v134, v130, 6 bitop3:0x6c
	v_lshlrev_b32_e32 v140, 4, v140
	v_lshlrev_b32_e32 v129, 4, v129
	v_add3_u32 v185, v135, v140, v133
	v_bitop3_b32 v140, v134, v138, 6 bitop3:0x6c
	v_bitop3_b32 v138, v136, v138, 7 bitop3:0x6c
	v_add3_u32 v190, v137, v129, v133
	v_bitop3_b32 v129, v136, v130, 7 bitop3:0x6c
	v_and_b32_e32 v128, 1, v128
	v_lshlrev_b32_e32 v140, 4, v140
	v_lshlrev_b32_e32 v138, 4, v138
	v_lshlrev_b32_e32 v129, 4, v129
	v_lshlrev_b32_e32 v130, 2, v128
	v_and_b32_e32 v131, 7, v173
	v_add3_u32 v186, v137, v140, v133
	v_add3_u32 v187, v139, v138, v133
	v_add3_u32 v191, v139, v129, v133
	v_bitop3_b32 v132, v130, v173, 7 bitop3:0x78
	v_bitop3_b32 v133, v130, v131, 1 bitop3:0x36
	v_bitop3_b32 v134, v130, v131, 2 bitop3:0x36
	v_bitop3_b32 v130, v130, v131, 3 bitop3:0x36
	v_readlane_b32 s58, v254, 56
	v_readlane_b32 s0, v254, 53
	v_lshl_add_u32 v129, v173, 7, s4
	v_lshlrev_b32_e32 v132, 4, v132
	v_lshlrev_b32_e32 v133, 4, v133
	v_lshlrev_b32_e32 v134, 4, v134
	v_lshlrev_b32_e32 v130, 4, v130
	v_readlane_b32 s47, v254, 55
	v_readlane_b32 s59, v254, 57
	v_readlane_b32 s1, v254, 54
	v_or_b32_e32 v192, 1, v174
	v_or_b32_e32 v193, 2, v174
	v_add_u32_e32 v194, 32, v174
	v_add_u32_e32 v195, 33, v174
	v_add_u32_e32 v196, 34, v174
	v_add_u32_e32 v197, 32, v175
	v_add_u32_e32 v198, 64, v174
	v_add_u32_e32 v199, 0x41, v174
	v_add_u32_e32 v200, 0x42, v174
	v_add_u32_e32 v201, 64, v175
	v_add_u32_e32 v202, 0x60, v174
	v_add_u32_e32 v203, 0x61, v174
	v_add_u32_e32 v204, 0x62, v174
	v_add_u32_e32 v205, 0x60, v175
	v_lshlrev_b32_e32 v148, 6, v128
	v_mov_b32_e32 v149, v145
	s_lshl_b32 s9, s47, 5
	s_lshl_b32 s38, s15, 5
	s_lshl_b32 s36, s47, 2
	s_lshl_b32 s8, s15, 2
	v_add_u32_e32 v206, v129, v132
	v_add_u32_e32 v207, v129, v133
	v_add_u32_e32 v208, v129, v134
	v_add_u32_e32 v209, v129, v130
	s_mov_b32 s56, s76
	s_mov_b32 s57, s0
	v_mov_b32_e32 v150, v152
	s_mov_b64 s[0:1], s[58:59]
	v_mov_b32_e32 v211, v152
	s_waitcnt vmcnt(16)
	s_branch .LBB7_460

; #define LAS __attribute__((address_space(3)))
; #define LDS_WAIT() asm volatile("s_waitcnt lgkmcnt(0)" ::: "memory")
; __device__ __forceinline__ float cl448(float v) { return fminf(fmaxf(v, -448.0f), 448.0f); }
; __device__ __forceinline__ void f8_pack(const f32x4 (&v)[16], LAS float* scr, int lane) {
;     LAS unsigned* su = (LAS unsigned*)scr; const int nq = lane & 7, kg = lane >> 3;
; #pragma unroll
;     for (int i2 = 0; i2 < 4; ++i2)
; #pragma unroll
;         for (int x = 0; x < 4; ++x) { const int r = 4 * nq + x, chunk = 2 * i2 + (kg >> 2);
;             su[r * 32 + ((chunk ^ (r & 7)) << 2) + (kg & 3)] = pg8::pk4_fp8(cl448(8.0f * v[4 * i2][x]), cl448(8.0f * v[4 * i2 + 1][x]), cl448(8.0f * v[4 * i2 + 2][x]), cl448(8.0f * v[4 * i2 + 3][x])); }
;     LDS_WAIT(); asm volatile("" ::: "memory");
; }
; __device__ __forceinline__ void f8_share(const P& p, LAS unsigned char* ring, int G, int vcu, int wave) {
;     ...
;     while (it < NF8) {
;         { const F8Item cur = ia; f8_pack(va, scr, lane); if (it + 2 * NGW < NF8) { ia = f8_item(p, it + 2 * NGW); f8_load(ia, va, lane); } f8_store(cur, scr, lane); }
.LBB7_460:
	s_waitcnt vmcnt(24)
	v_mul_f32_e32 v128, 0x41000000, v0
	v_med3_f32 v129, v128, s96, v154
	s_waitcnt lgkmcnt(1)
	v_mul_f32_e32 v128, 0x41000000, v4
	v_med3_f32 v130, v128, s96, v154
	v_mul_f32_e32 v128, 0x41000000, v8
	v_med3_f32 v131, v128, s96, v154
	v_mul_f32_e32 v128, 0x41000000, v12
	v_med3_f32 v132, v128, s96, v154
	s_add_i32 s11, s47, s15
	v_mov_b32_e32 v133, v128
	v_cvt_pk_fp8_f32 v133, v129, v130
	v_mul_f32_e32 v129, 0x41000000, v1
	s_waitcnt lgkmcnt(0)
	v_mul_f32_e32 v130, 0x41000000, v5
	v_med3_f32 v129, v129, s96, v154
	v_cvt_pk_fp8_f32 v133, v131, v132 op_sel:[0,0,1]
	v_med3_f32 v130, v130, s96, v154
	v_mul_f32_e32 v131, 0x41000000, v9
	v_mul_f32_e32 v132, 0x41000000, v13
	ds_write_b32 v176, v133
	v_mov_b32_e32 v133, v128
	v_cvt_pk_fp8_f32 v133, v129, v130
	v_med3_f32 v131, v131, s96, v154
	v_med3_f32 v132, v132, s96, v154
	v_mul_f32_e32 v129, 0x41000000, v2
	v_cvt_pk_fp8_f32 v133, v131, v132 op_sel:[0,0,1]
	v_mul_f32_e32 v130, 0x41000000, v6
	v_med3_f32 v129, v129, s96, v154
	v_med3_f32 v130, v130, s96, v154
	ds_write_b32 v177, v133
	v_mov_b32_e32 v133, v128
	v_cvt_pk_fp8_f32 v133, v129, v130
	v_mul_f32_e32 v131, 0x41000000, v10
	v_mul_f32_e32 v132, 0x41000000, v14
	v_med3_f32 v131, v131, s96, v154
	v_med3_f32 v132, v132, s96, v154
	v_cvt_pk_fp8_f32 v133, v131, v132 op_sel:[0,0,1]
	v_mul_f32_e32 v129, 0x41000000, v3
	v_mul_f32_e32 v130, 0x41000000, v7
	v_med3_f32 v129, v129, s96, v154
	ds_write_b32 v178, v133
	v_med3_f32 v130, v130, s96, v154
	v_mov_b32_e32 v133, v128
	v_cvt_pk_fp8_f32 v133, v129, v130
	v_mul_f32_e32 v131, 0x41000000, v11
	v_mul_f32_e32 v132, 0x41000000, v15
	v_med3_f32 v131, v131, s96, v154
	v_med3_f32 v132, v132, s96, v154
	v_cvt_pk_fp8_f32 v133, v131, v132 op_sel:[0,0,1]
	v_mul_f32_e32 v129, 0x41000000, v16
	v_mul_f32_e32 v130, 0x41000000, v20
	v_med3_f32 v129, v129, s96, v154
	ds_write_b32 v179, v133
	v_med3_f32 v130, v130, s96, v154
	v_mov_b32_e32 v133, v128
	v_cvt_pk_fp8_f32 v133, v129, v130
	v_mul_f32_e32 v131, 0x41000000, v24
	v_mul_f32_e32 v132, 0x41000000, v28
	v_med3_f32 v131, v131, s96, v154
	v_med3_f32 v132, v132, s96, v154
	v_cvt_pk_fp8_f32 v133, v131, v132 op_sel:[0,0,1]
	v_mul_f32_e32 v129, 0x41000000, v17
	v_mul_f32_e32 v130, 0x41000000, v21
	v_med3_f32 v129, v129, s96, v154
	ds_write_b32 v180, v133
	v_med3_f32 v130, v130, s96, v154
	v_mov_b32_e32 v133, v128
	v_cvt_pk_fp8_f32 v133, v129, v130
	v_mul_f32_e32 v131, 0x41000000, v25
	v_mul_f32_e32 v132, 0x41000000, v29
	v_med3_f32 v131, v131, s96, v154
	v_med3_f32 v132, v132, s96, v154
	v_cvt_pk_fp8_f32 v133, v131, v132 op_sel:[0,0,1]
	v_mul_f32_e32 v129, 0x41000000, v18
	v_mul_f32_e32 v130, 0x41000000, v22
	v_med3_f32 v129, v129, s96, v154
	ds_write_b32 v181, v133
	v_med3_f32 v130, v130, s96, v154
	v_mov_b32_e32 v133, v128
	v_cvt_pk_fp8_f32 v133, v129, v130
	v_mul_f32_e32 v131, 0x41000000, v26
	v_mul_f32_e32 v132, 0x41000000, v30
	v_med3_f32 v131, v131, s96, v154
	v_med3_f32 v132, v132, s96, v154
	v_cvt_pk_fp8_f32 v133, v131, v132 op_sel:[0,0,1]
	v_mul_f32_e32 v129, 0x41000000, v19
	v_mul_f32_e32 v130, 0x41000000, v23
	v_med3_f32 v129, v129, s96, v154
	ds_write_b32 v182, v133
	v_med3_f32 v130, v130, s96, v154
	v_mov_b32_e32 v133, v128
	v_cvt_pk_fp8_f32 v133, v129, v130
	v_mul_f32_e32 v131, 0x41000000, v27
	v_mul_f32_e32 v132, 0x41000000, v31
	v_med3_f32 v131, v131, s96, v154
	v_med3_f32 v132, v132, s96, v154
	v_cvt_pk_fp8_f32 v133, v131, v132 op_sel:[0,0,1]
	v_mul_f32_e32 v129, 0x41000000, v32
	v_mul_f32_e32 v130, 0x41000000, v36
	v_med3_f32 v129, v129, s96, v154
	ds_write_b32 v183, v133
	v_med3_f32 v130, v130, s96, v154
	v_mov_b32_e32 v133, v128
	v_cvt_pk_fp8_f32 v133, v129, v130
	v_mul_f32_e32 v131, 0x41000000, v40
	v_mul_f32_e32 v132, 0x41000000, v44
	v_med3_f32 v131, v131, s96, v154
	v_med3_f32 v132, v132, s96, v154
	v_cvt_pk_fp8_f32 v133, v131, v132 op_sel:[0,0,1]
	v_mul_f32_e32 v129, 0x41000000, v33
	v_mul_f32_e32 v130, 0x41000000, v37
	v_med3_f32 v129, v129, s96, v154
	ds_write_b32 v184, v133
	v_med3_f32 v130, v130, s96, v154
	v_mov_b32_e32 v133, v128
	v_cvt_pk_fp8_f32 v133, v129, v130
	v_mul_f32_e32 v131, 0x41000000, v41
	v_mul_f32_e32 v132, 0x41000000, v45
	v_med3_f32 v131, v131, s96, v154
	v_med3_f32 v132, v132, s96, v154
	v_cvt_pk_fp8_f32 v133, v131, v132 op_sel:[0,0,1]
	v_mul_f32_e32 v129, 0x41000000, v34
	v_mul_f32_e32 v130, 0x41000000, v38
	v_med3_f32 v129, v129, s96, v154
	ds_write_b32 v185, v133
	v_med3_f32 v130, v130, s96, v154
	v_mov_b32_e32 v133, v128
	v_cvt_pk_fp8_f32 v133, v129, v130
	v_mul_f32_e32 v131, 0x41000000, v42
	v_mul_f32_e32 v132, 0x41000000, v46
	v_med3_f32 v131, v131, s96, v154
	v_med3_f32 v132, v132, s96, v154
	v_cvt_pk_fp8_f32 v133, v131, v132 op_sel:[0,0,1]
	v_mul_f32_e32 v129, 0x41000000, v35
	v_mul_f32_e32 v130, 0x41000000, v39
	v_med3_f32 v129, v129, s96, v154
	ds_write_b32 v186, v133
	v_med3_f32 v130, v130, s96, v154
	v_mov_b32_e32 v133, v128
	v_cvt_pk_fp8_f32 v133, v129, v130
	v_mul_f32_e32 v131, 0x41000000, v43
	v_mul_f32_e32 v132, 0x41000000, v47
	v_med3_f32 v131, v131, s96, v154
	v_med3_f32 v132, v132, s96, v154
	v_cvt_pk_fp8_f32 v133, v131, v132 op_sel:[0,0,1]
	v_mul_f32_e32 v129, 0x41000000, v48
	v_mul_f32_e32 v130, 0x41000000, v52
	v_med3_f32 v129, v129, s96, v154
	ds_write_b32 v187, v133
	v_med3_f32 v130, v130, s96, v154
	v_mov_b32_e32 v133, v128
	v_cvt_pk_fp8_f32 v133, v129, v130
	v_mul_f32_e32 v131, 0x41000000, v64
	v_mul_f32_e32 v132, 0x41000000, v68
	v_med3_f32 v131, v131, s96, v154
	v_med3_f32 v132, v132, s96, v154
	v_cvt_pk_fp8_f32 v133, v131, v132 op_sel:[0,0,1]
	v_mul_f32_e32 v129, 0x41000000, v49
	v_mul_f32_e32 v130, 0x41000000, v53
	v_med3_f32 v129, v129, s96, v154
	ds_write_b32 v188, v133
	v_med3_f32 v130, v130, s96, v154
	v_mov_b32_e32 v133, v128
	v_cvt_pk_fp8_f32 v133, v129, v130
	v_mul_f32_e32 v131, 0x41000000, v65
	v_mul_f32_e32 v132, 0x41000000, v69
	v_med3_f32 v131, v131, s96, v154
	v_med3_f32 v132, v132, s96, v154
	v_cvt_pk_fp8_f32 v133, v131, v132 op_sel:[0,0,1]
	v_mul_f32_e32 v129, 0x41000000, v50
	v_mul_f32_e32 v130, 0x41000000, v54
	v_med3_f32 v129, v129, s96, v154
	ds_write_b32 v189, v133
	v_med3_f32 v130, v130, s96, v154
	v_mov_b32_e32 v133, v128
	v_cvt_pk_fp8_f32 v133, v129, v130
	v_mul_f32_e32 v129, 0x41000000, v51
	v_mul_f32_e32 v130, 0x41000000, v55
	v_med3_f32 v129, v129, s96, v154
	v_med3_f32 v130, v130, s96, v154
	v_mul_f32_e32 v131, 0x41000000, v66
	v_mul_f32_e32 v132, 0x41000000, v70
	v_cvt_pk_fp8_f32 v128, v129, v130
	v_med3_f32 v131, v131, s96, v154
	v_med3_f32 v132, v132, s96, v154
	v_cvt_pk_fp8_f32 v133, v131, v132 op_sel:[0,0,1]
	v_mul_f32_e32 v131, 0x41000000, v67
	v_mul_f32_e32 v132, 0x41000000, v71
	v_med3_f32 v131, v131, s96, v154
	v_med3_f32 v132, v132, s96, v154
	v_cvt_pk_fp8_f32 v128, v131, v132 op_sel:[0,0,1]
	ds_write_b32 v190, v133
	s_cmpk_gt_i32 s11, 0x5fff
	s_cselect_b64 s[50:51], -1, 0
	ds_write_b32 v191, v128
	s_waitcnt lgkmcnt(0)
	s_and_b64 vcc, exec, s[50:51]
	s_mov_b32 s86, s56
	s_mov_b32 s54, s57
	s_cbranch_vccnz .Lf8b_skip_a
; __device__ __forceinline__ F8Item f8_item(const P& p, int r) {
;     constexpr int I_W1 = 8 * 64, I_W2 = 8 * 32; F8Item it;
;     if (r < NE * I_W1) { const int e = r / I_W1, q = r % I_W1; it.W = p.w1 + (size_t)e * DM * 2048; it.WT = p.ws + WS_W1T + (size_t)e * 2048 * DM; it.N = 2048; it.k0 = 128 * (q / 64); it.n0 = 32 * (q % 64); it.map = 1; }
;     else { r -= NE * I_W1; const int e = r / I_W2, q = r % I_W2; it.W = p.w2 + (size_t)e * DM * DM; it.WT = p.ws + WS_W2T + (size_t)e * DM * DM; it.N = DM; it.k0 = 128 * (q / 32); it.n0 = 32 * (q % 32); it.map = 0; }
;     return it;
; }
; __device__ __forceinline__ void f8_share(const P& p, LAS unsigned char* ring, int G, int vcu, int wave) {
;     ...
;         { const F8Item cur = ia; f8_pack(va, scr, lane); if (it + 2 * NGW < NF8) { ia = f8_item(p, it + 2 * NGW); f8_load(ia, va, lane); } f8_store(cur, scr, lane); }
	s_cmpk_gt_i32 s11, 0x3fff
	s_mov_b64 s[62:63], -1
	s_cbranch_scc0 .LBB7_463
	s_add_i32 s0, s11, 0xffffc000
	s_lshr_b32 s6, s0, 8
	s_lshl_b64 s[0:1], s[6:7], 20
	s_lshl_b64 s[54:55], s[6:7], 22
	s_add_u32 s60, s24, s54
	s_addc_u32 s61, s25, s55
	s_add_u32 s0, s89, s0
	s_addc_u32 s1, s94, s1
	s_add_i32 s6, s8, s36
	s_and_b32 s86, s6, 0x380
	s_add_i32 s6, s38, s9
	s_and_b32 s54, s6, 0x3e0
	s_mov_b64 s[62:63], 0

; #define LAS __attribute__((address_space(3)))
; #define LDS_WAIT() asm volatile("s_waitcnt lgkmcnt(0)" ::: "memory")
; __device__ __forceinline__ int rmap_w2(int c) { const int cc = c & 255; return (c & ~255) + 128 * ((cc >> 3) & 1) + 32 * (cc >> 6) + 8 * ((cc >> 4) & 3) + (cc & 7); }
; __device__ __forceinline__ void f8_store(const F8Item& it, LAS float* scr, int lane) {
;     const LAS unsigned* su = (const LAS unsigned*)scr; const int n = lane >> 1, half = lane & 1;
;     u32x4 o[4];
; #pragma unroll
;     for (int q = 0; q < 4; ++q) o[q] = *(const LAS u32x4*)(su + n * 32 + (((4 * half + q) ^ (n & 7)) << 2));
;     const int src = it.n0 + n; const int row = it.map ? rmap_w1(src) : rmap_w2(src); unsigned char* dst = it.WT + (size_t)row * DM + it.k0 + 64 * half;
; #pragma unroll
;     for (int q = 0; q < 4; ++q) *(u32x4*)(dst + 16 * q) = o[q];
;     LDS_WAIT(); asm volatile("" ::: "memory");
; }
; __device__ __forceinline__ void f8_share(const P& p, LAS unsigned char* ring, int G, int vcu, int wave) {
;     ...
;         if (it + NGW >= NF8) break;
;         { const F8Item cur = ib; f8_pack(vb, scr, lane); if (it + 3 * NGW < NF8) { ib = f8_item(p, it + 3 * NGW); f8_load(ib, vb, lane); } f8_store(cur, scr, lane); }
.LBB7_470:
	v_ashrrev_i32_e32 v151, 31, v150
	v_lshlrev_b64 v[150:151], 10, v[150:151]
	v_lshl_add_u64 v[150:151], s[58:59], 0, v[150:151]
	s_ashr_i32 s57, s56, 31
	v_lshl_add_u64 v[150:151], v[150:151], 0, s[56:57]
	v_lshl_add_u64 v[150:151], v[150:151], 0, v[148:149]
	s_waitcnt lgkmcnt(3)
	global_store_dwordx4 v[150:151], v[128:131], off
	s_waitcnt lgkmcnt(2)
	global_store_dwordx4 v[150:151], v[132:135], off offset:16
	s_waitcnt lgkmcnt(1)
	global_store_dwordx4 v[150:151], v[136:139], off offset:32
	s_waitcnt lgkmcnt(0)
	global_store_dwordx4 v[150:151], v[140:143], off offset:48
	s_waitcnt lgkmcnt(0)
	s_add_i32 s6, s14, s47
	s_cmpk_gt_i32 s6, 0x5fff
	s_cbranch_scc1 .LBB7_458
	s_waitcnt vmcnt(20)
	v_mul_f32_e32 v128, 0x41000000, v56
	v_med3_f32 v129, v128, s96, v154
	v_mul_f32_e32 v128, 0x41000000, v60
	v_med3_f32 v130, v128, s96, v154
	v_mul_f32_e32 v128, 0x41000000, v72
	v_med3_f32 v131, v128, s96, v154
	v_mul_f32_e32 v128, 0x41000000, v76
	v_med3_f32 v132, v128, s96, v154
	s_mul_i32 s6, s3, 24
	v_mov_b32_e32 v133, v128
	v_cvt_pk_fp8_f32 v133, v129, v130
	v_mul_f32_e32 v129, 0x41000000, v57
	v_mul_f32_e32 v130, 0x41000000, v61
	v_med3_f32 v129, v129, s96, v154
	v_cvt_pk_fp8_f32 v133, v131, v132 op_sel:[0,0,1]
	v_med3_f32 v130, v130, s96, v154
	v_mul_f32_e32 v131, 0x41000000, v73
	v_mul_f32_e32 v132, 0x41000000, v77
	ds_write_b32 v176, v133
	v_mov_b32_e32 v133, v128
	v_cvt_pk_fp8_f32 v133, v129, v130
	v_med3_f32 v131, v131, s96, v154
	v_med3_f32 v132, v132, s96, v154
	v_mul_f32_e32 v129, 0x41000000, v58
	v_cvt_pk_fp8_f32 v133, v131, v132 op_sel:[0,0,1]
	v_mul_f32_e32 v130, 0x41000000, v62
	v_med3_f32 v129, v129, s96, v154
	v_med3_f32 v130, v130, s96, v154
	ds_write_b32 v177, v133
	v_mov_b32_e32 v133, v128
	v_cvt_pk_fp8_f32 v133, v129, v130
	v_mul_f32_e32 v131, 0x41000000, v74
	v_mul_f32_e32 v132, 0x41000000, v78
	v_med3_f32 v131, v131, s96, v154
	v_med3_f32 v132, v132, s96, v154
	v_cvt_pk_fp8_f32 v133, v131, v132 op_sel:[0,0,1]
	v_mul_f32_e32 v129, 0x41000000, v59
	v_mul_f32_e32 v130, 0x41000000, v63
	v_med3_f32 v129, v129, s96, v154
	ds_write_b32 v178, v133
	v_med3_f32 v130, v130, s96, v154
	v_mov_b32_e32 v133, v128
	v_cvt_pk_fp8_f32 v133, v129, v130
	v_mul_f32_e32 v131, 0x41000000, v75
	v_mul_f32_e32 v132, 0x41000000, v79
	v_med3_f32 v131, v131, s96, v154
	v_med3_f32 v132, v132, s96, v154
	v_cvt_pk_fp8_f32 v133, v131, v132 op_sel:[0,0,1]
	v_mul_f32_e32 v129, 0x41000000, v80
	v_mul_f32_e32 v130, 0x41000000, v84
	v_med3_f32 v129, v129, s96, v154
	ds_write_b32 v179, v133
	v_med3_f32 v130, v130, s96, v154
	v_mov_b32_e32 v133, v128
	v_cvt_pk_fp8_f32 v133, v129, v130
	v_mul_f32_e32 v131, 0x41000000, v88
	v_mul_f32_e32 v132, 0x41000000, v92
	v_med3_f32 v131, v131, s96, v154
	v_med3_f32 v132, v132, s96, v154
	v_cvt_pk_fp8_f32 v133, v131, v132 op_sel:[0,0,1]
	v_mul_f32_e32 v129, 0x41000000, v81
	v_mul_f32_e32 v130, 0x41000000, v85
	v_med3_f32 v129, v129, s96, v154
	ds_write_b32 v180, v133
	v_med3_f32 v130, v130, s96, v154
	v_mov_b32_e32 v133, v128
	v_cvt_pk_fp8_f32 v133, v129, v130
	v_mul_f32_e32 v131, 0x41000000, v89
	v_mul_f32_e32 v132, 0x41000000, v93
	v_med3_f32 v131, v131, s96, v154
	v_med3_f32 v132, v132, s96, v154
	v_cvt_pk_fp8_f32 v133, v131, v132 op_sel:[0,0,1]
	v_mul_f32_e32 v129, 0x41000000, v82
	v_mul_f32_e32 v130, 0x41000000, v86
	v_med3_f32 v129, v129, s96, v154
	ds_write_b32 v181, v133
	v_med3_f32 v130, v130, s96, v154
	v_mov_b32_e32 v133, v128
	v_cvt_pk_fp8_f32 v133, v129, v130
	v_mul_f32_e32 v131, 0x41000000, v90
	v_mul_f32_e32 v132, 0x41000000, v94
	v_med3_f32 v131, v131, s96, v154
	v_med3_f32 v132, v132, s96, v154
	v_cvt_pk_fp8_f32 v133, v131, v132 op_sel:[0,0,1]
	v_mul_f32_e32 v129, 0x41000000, v83
	v_mul_f32_e32 v130, 0x41000000, v87
	v_med3_f32 v129, v129, s96, v154
	ds_write_b32 v182, v133
	v_med3_f32 v130, v130, s96, v154
	v_mov_b32_e32 v133, v128
	v_cvt_pk_fp8_f32 v133, v129, v130
	v_mul_f32_e32 v131, 0x41000000, v91
	v_mul_f32_e32 v132, 0x41000000, v95
	v_med3_f32 v131, v131, s96, v154
	v_med3_f32 v132, v132, s96, v154
	v_cvt_pk_fp8_f32 v133, v131, v132 op_sel:[0,0,1]
; #define LAS __attribute__((address_space(3)))
; #define LDS_WAIT() asm volatile("s_waitcnt lgkmcnt(0)" ::: "memory")
; __device__ __forceinline__ float cl448(float v) { return fminf(fmaxf(v, -448.0f), 448.0f); }
; __device__ __forceinline__ void f8_pack(const f32x4 (&v)[16], LAS float* scr, int lane) {
;     LAS unsigned* su = (LAS unsigned*)scr; const int nq = lane & 7, kg = lane >> 3;
; #pragma unroll
;     for (int i2 = 0; i2 < 4; ++i2)
; #pragma unroll
;         for (int x = 0; x < 4; ++x) { const int r = 4 * nq + x, chunk = 2 * i2 + (kg >> 2);
;             su[r * 32 + ((chunk ^ (r & 7)) << 2) + (kg & 3)] = pg8::pk4_fp8(cl448(8.0f * v[4 * i2][x]), cl448(8.0f * v[4 * i2 + 1][x]), cl448(8.0f * v[4 * i2 + 2][x]), cl448(8.0f * v[4 * i2 + 3][x])); }
;     LDS_WAIT(); asm volatile("" ::: "memory");
; }
; __device__ __forceinline__ void f8_share(const P& p, LAS unsigned char* ring, int G, int vcu, int wave) {
;     ...
;         { const F8Item cur = ib; f8_pack(vb, scr, lane); if (it + 3 * NGW < NF8) { ib = f8_item(p, it + 3 * NGW); f8_load(ib, vb, lane); } f8_store(cur, scr, lane); }
;         it += 2 * NGW;
	v_mul_f32_e32 v129, 0x41000000, v96
	v_mul_f32_e32 v130, 0x41000000, v100
	v_med3_f32 v129, v129, s96, v154
	ds_write_b32 v183, v133
	v_med3_f32 v130, v130, s96, v154
	v_mov_b32_e32 v133, v128
	v_cvt_pk_fp8_f32 v133, v129, v130
	v_mul_f32_e32 v131, 0x41000000, v104
	v_mul_f32_e32 v132, 0x41000000, v108
	v_med3_f32 v131, v131, s96, v154
	v_med3_f32 v132, v132, s96, v154
	v_cvt_pk_fp8_f32 v133, v131, v132 op_sel:[0,0,1]
	v_mul_f32_e32 v129, 0x41000000, v97
	v_mul_f32_e32 v130, 0x41000000, v101
	v_med3_f32 v129, v129, s96, v154
	ds_write_b32 v184, v133
	v_med3_f32 v130, v130, s96, v154
	v_mov_b32_e32 v133, v128
	v_cvt_pk_fp8_f32 v133, v129, v130
	v_mul_f32_e32 v131, 0x41000000, v105
	v_mul_f32_e32 v132, 0x41000000, v109
	v_med3_f32 v131, v131, s96, v154
	v_med3_f32 v132, v132, s96, v154
	v_cvt_pk_fp8_f32 v133, v131, v132 op_sel:[0,0,1]
	v_mul_f32_e32 v129, 0x41000000, v98
	v_mul_f32_e32 v130, 0x41000000, v102
	v_med3_f32 v129, v129, s96, v154
	ds_write_b32 v185, v133
	v_med3_f32 v130, v130, s96, v154
	v_mov_b32_e32 v133, v128
	v_cvt_pk_fp8_f32 v133, v129, v130
	v_mul_f32_e32 v131, 0x41000000, v106
	v_mul_f32_e32 v132, 0x41000000, v110
	v_med3_f32 v131, v131, s96, v154
	v_med3_f32 v132, v132, s96, v154
	v_cvt_pk_fp8_f32 v133, v131, v132 op_sel:[0,0,1]
	v_mul_f32_e32 v129, 0x41000000, v99
	v_mul_f32_e32 v130, 0x41000000, v103
	v_med3_f32 v129, v129, s96, v154
	ds_write_b32 v186, v133
	v_med3_f32 v130, v130, s96, v154
	v_mov_b32_e32 v133, v128
	v_cvt_pk_fp8_f32 v133, v129, v130
	v_mul_f32_e32 v131, 0x41000000, v107
	v_mul_f32_e32 v132, 0x41000000, v111
	v_med3_f32 v131, v131, s96, v154
	v_med3_f32 v132, v132, s96, v154
	v_cvt_pk_fp8_f32 v133, v131, v132 op_sel:[0,0,1]
	v_mul_f32_e32 v129, 0x41000000, v112
	v_mul_f32_e32 v130, 0x41000000, v116
	v_med3_f32 v129, v129, s96, v154
	ds_write_b32 v187, v133
	v_med3_f32 v130, v130, s96, v154
	v_mov_b32_e32 v133, v128
	v_cvt_pk_fp8_f32 v133, v129, v130
	v_mul_f32_e32 v131, 0x41000000, v120
	v_mul_f32_e32 v132, 0x41000000, v124
	v_med3_f32 v131, v131, s96, v154
	v_med3_f32 v132, v132, s96, v154
	v_cvt_pk_fp8_f32 v133, v131, v132 op_sel:[0,0,1]
	v_mul_f32_e32 v129, 0x41000000, v113
	v_mul_f32_e32 v130, 0x41000000, v117
	v_med3_f32 v129, v129, s96, v154
	ds_write_b32 v188, v133
	v_med3_f32 v130, v130, s96, v154
	v_mov_b32_e32 v133, v128
	v_cvt_pk_fp8_f32 v133, v129, v130
	v_mul_f32_e32 v131, 0x41000000, v121
	v_mul_f32_e32 v132, 0x41000000, v125
	v_med3_f32 v131, v131, s96, v154
	v_med3_f32 v132, v132, s96, v154
	v_cvt_pk_fp8_f32 v133, v131, v132 op_sel:[0,0,1]
	v_mul_f32_e32 v129, 0x41000000, v114
	v_mul_f32_e32 v130, 0x41000000, v118
	v_med3_f32 v129, v129, s96, v154
	ds_write_b32 v189, v133
	v_med3_f32 v130, v130, s96, v154
	v_mov_b32_e32 v133, v128
	v_cvt_pk_fp8_f32 v133, v129, v130
	v_mul_f32_e32 v129, 0x41000000, v115
	v_mul_f32_e32 v130, 0x41000000, v119
	v_med3_f32 v129, v129, s96, v154
	v_med3_f32 v130, v130, s96, v154
	v_mul_f32_e32 v131, 0x41000000, v122
	v_mul_f32_e32 v132, 0x41000000, v126
	v_cvt_pk_fp8_f32 v128, v129, v130
	v_med3_f32 v131, v131, s96, v154
	v_med3_f32 v132, v132, s96, v154
	v_cvt_pk_fp8_f32 v133, v131, v132 op_sel:[0,0,1]
	v_mul_f32_e32 v131, 0x41000000, v123
	v_mul_f32_e32 v132, 0x41000000, v127
	v_med3_f32 v131, v131, s96, v154
	v_med3_f32 v132, v132, s96, v154
	v_cvt_pk_fp8_f32 v128, v131, v132 op_sel:[0,0,1]
	ds_write_b32 v190, v133
	s_add_i32 s47, s6, s47
	s_cmpk_gt_i32 s47, 0x5fff
	ds_write_b32 v191, v128
	s_waitcnt lgkmcnt(0)
	s_mov_b64 s[56:57], s[48:49]
	s_mov_b32 s6, s46
	s_mov_b32 s58, s37
	v_mov_b32_e32 v144, v210
	s_cbranch_scc1 .Lf8b_skip_b
	s_cmpk_gt_i32 s47, 0x3fff
	s_mov_b64 s[62:63], -1
	s_cbranch_scc0 .LBB7_474
	s_add_i32 s6, s47, 0xffffc000
	s_lshr_b32 s6, s6, 8
	s_lshl_b64 s[56:57], s[6:7], 20
	s_lshl_b64 s[58:59], s[6:7], 22
	s_add_u32 s60, s24, s58
	s_addc_u32 s61, s25, s59
	s_add_u32 s56, s89, s56
	s_mul_i32 s6, s3, 0x60
	s_mul_i32 s55, s3, 0x300
	s_addc_u32 s57, s94, s57
	s_add_i32 s6, s6, s36
	s_add_i32 s55, s55, s9
	s_and_b32 s6, s6, 0x380
	s_and_b32 s58, s55, 0x3e0
	s_mov_b64 s[62:63], 0

; #define LAS __attribute__((address_space(3)))
; __device__ __forceinline__ int fresh_lane() { unsigned z = 0u; asm volatile("" : "+v"(z)); return (int)__builtin_amdgcn_mbcnt_hi(~0u, __builtin_amdgcn_mbcnt_lo(~0u, z)); }
;     __device__ __forceinline__ void a_offsets(const Unit& u, int wid, unsigned (&o)[2][2]) const {
;         int R0, C0; stage_rc((wid * 64 + fresh_lane()) * 16, R0, C0);
; #pragma unroll
;         for (int h = 0; h < 2; ++h)
; #pragma unroll
;             for (int i = 0; i < 2; ++i) {
;                 if (GATHER) { int pos = u.pos0 + R0 + 64 * i + 128 * h; pos = pos < u.cnt ? pos : u.cnt - 1; const int tk = extok[u.e * 65536 + pos]; o[h][i] = (unsigned)(tk >> 2) * (unsigned)PITCH + (unsigned)C0 * 2u; }
;                 else o[h][i] = (unsigned)((R0 + 64 * i + 128 * h) * PITCH + C0 * 2); }
;     }
; template <class Epi, class Sched>
; __device__ __forceinline__ void gemm_phase(LAS unsigned char* lds, const Sched& S, const Epi& E, const int wid) {
;     ...
;         const bool has_next = S.next(ui + 1, nxt);
;         const char* nA = has_next ? S.aptr(nxt) : cA; const char* nB = has_next ? S.bptr(nxt) : cB;
;         if constexpr (Sched::GATHERS) {
;             if (has_next) S.a_offsets(nxt, wid, gn);
;             else {
; #pragma unroll
;                 for (int h = 0; h < 2; ++h)
; #pragma unroll
;                     for (int i = 0; i < 2; ++i) gn[h][i] = gc[h][i]; }
;             *(LAS u32x4*)(lds + (TAB_GOFF - RING_OFF) + tid * 16) = (u32x4){gn[0][0], gn[0][1], gn[1][0], gn[1][1]}; }
.LBB7_776:
	v_cndmask_b32_e64 v64, 0, 1, s[46:47]
	v_cmp_ne_u32_e64 s[0:1], 1, v64
	s_andn2_b64 vcc, exec, s[46:47]
	s_waitcnt lgkmcnt(0)
	v_mov_b32_e32 v67, v115
	v_mov_b32_e32 v66, v114
	v_mov_b32_e32 v65, v113
	v_mov_b32_e32 v64, v112
	s_mov_b32 s98, 0
	s_cbranch_vccnz .LBB7_778
	s_mov_b32 s98, 1
	v_mov_b32_e32 v64, 0
	s_add_i32 s37, s71, -1
	v_mbcnt_lo_u32_b32 v64, -1, v64
	v_mbcnt_hi_u32_b32 v64, -1, v64
	v_lshl_add_u32 v64, v64, 4, s21
	v_ashrrev_i32_e32 v65, 31, v64
	v_lshrrev_b32_e32 v65, 22, v65
	v_add_u32_e32 v65, v64, v65
	v_ashrrev_i32_e32 v74, 10, v65
	v_mul_i32_i24_e32 v65, 0x400, v74
	v_sub_u32_e32 v64, v64, v65
	v_lshrrev_b32_e32 v65, 4, v64
	v_bitop3_b32 v75, v65, v64, 32 bitop3:0x6c
	v_ashrrev_i32_e32 v65, 31, v75
	v_lshrrev_b32_e32 v65, 26, v65
	v_lshlrev_b32_e32 v64, 3, v74
	v_add_u32_e32 v80, v75, v65
	v_and_b32_e32 v64, -16, v64
	v_ashrrev_i32_e32 v65, 6, v80
	v_add3_u32 v72, v65, v64, s72
	v_min_i32_e32 v64, s37, v72
	s_lshl_b32 s39, s36, 16
	v_add_u32_e32 v64, s39, v64
	v_ashrrev_i32_e32 v65, 31, v64
	v_lshl_add_u64 v[64:65], v[64:65], 2, s[8:9]
	global_load_dword v155, v[64:65], off
	v_add_u32_e32 v64, 64, v72
	v_add_u32_e32 v66, 0x80, v72
	v_min_i32_e32 v64, s37, v64
	v_min_i32_e32 v66, s37, v66
	v_add_u32_e32 v72, 0xc0, v72
	v_add_u32_e32 v64, s39, v64
	v_add_u32_e32 v66, s39, v66
	v_min_i32_e32 v72, s37, v72
	v_ashrrev_i32_e32 v65, 31, v64
	v_ashrrev_i32_e32 v67, 31, v66
	v_add_u32_e32 v72, s39, v72
	v_lshl_add_u64 v[64:65], v[64:65], 2, s[8:9]
	v_lshl_add_u64 v[66:67], v[66:67], 2, s[8:9]
	v_ashrrev_i32_e32 v73, 31, v72
	v_lshl_add_u64 v[72:73], v[72:73], 2, s[8:9]
	global_load_dword v252, v[64:65], off
	s_nop 0
	global_load_dword v253, v[66:67], off
	s_nop 0
	global_load_dword v255, v[72:73], off

; #define LAS __attribute__((address_space(3)))
; __device__ __forceinline__ int fresh_lane() { unsigned z = 0u; asm volatile("" : "+v"(z)); return (int)__builtin_amdgcn_mbcnt_hi(~0u, __builtin_amdgcn_mbcnt_lo(~0u, z)); }
;     __device__ __forceinline__ void a_offsets(const Unit& u, int wid, unsigned (&o)[2][2]) const {
;         int R0, C0; stage_rc((wid * 64 + fresh_lane()) * 16, R0, C0);
; #pragma unroll
;         for (int h = 0; h < 2; ++h)
; #pragma unroll
;             for (int i = 0; i < 2; ++i) {
;                 if (GATHER) { int pos = u.pos0 + R0 + 64 * i + 128 * h; pos = pos < u.cnt ? pos : u.cnt - 1; const int tk = extok[u.e * 65536 + pos]; o[h][i] = (unsigned)(tk >> 2) * (unsigned)PITCH + (unsigned)C0 * 2u; }
;                 else o[h][i] = (unsigned)((R0 + 64 * i + 128 * h) * PITCH + C0 * 2); }
; template <class Epi, class Sched>
; __device__ __forceinline__ void gemm_phase(LAS unsigned char* lds, const Sched& S, const Epi& E, const int wid) {
;     ...
;             const char* a2 = last ? nA : cA + (size_t)(t + 2) * kstep; const char* b2 = last ? nB : cB + (size_t)(t + 2) * kstep;
;             const char* a3 = a2 + kstep; const char* b3 = b2 + kstep;
;             unsigned o2[2][2];
;             if constexpr (Sched::GATHERS) {
; #pragma unroll
;                 for (int h = 0; h < 2; ++h)
; #pragma unroll
;                     for (int i = 0; i < 2; ++i) o2[h][i] = gc[h][i];
;                 if (last) { const u32x4 g_ = *(const LAS u32x4*)(lds + (TAB_GOFF - RING_OFF) + tid * 16); o2[0][0] = g_.x; o2[0][1] = g_.y; o2[1][0] = g_.z; o2[1][1] = g_.w; } }
.LBB7_779:
	s_cmp_eq_u32 s78, 4
	s_cselect_b64 s[50:51], -1, 0
	s_cmp_lg_u32 s78, 4
	v_mov_b32_e32 v135, v115
	v_mov_b32_e32 v134, v114
	v_mov_b32_e32 v133, v113
	v_mov_b32_e32 v132, v112
	s_cbranch_scc1 .LBB7_781
	s_cmp_eq_u32 s98, 0
	s_cbranch_scc1 .Lp5_gn_parked
	v_and_b32_e32 v132, 0x3ff, v148
	v_lshrrev_b32_e32 v133, 4, v132
	v_and_b32_e32 v133, 32, v133
	v_xor_b32_e32 v132, v132, v133
	v_and_b32_e32 v132, 62, v132
	v_lshrrev_b32_e32 v133, 4, v148
	v_and_b32_e32 v133, 64, v133
	v_or_b32_e32 v135, v132, v133
	v_lshlrev_b32_e32 v132, 8, v155
	v_lshlrev_b32_e32 v133, 8, v252
	v_lshlrev_b32_e32 v134, 8, v253
	v_lshlrev_b32_e32 v255, 8, v255
	v_and_b32_e32 v132, 0xfffffc00, v132
	v_and_b32_e32 v133, 0xfffffc00, v133
	v_and_b32_e32 v134, 0xfffffc00, v134
	v_and_b32_e32 v255, 0xfffffc00, v255
	v_add_u32_e32 v132, v135, v132
	v_add_u32_e32 v133, v135, v133
	v_add_u32_e32 v134, v135, v134
	v_add_u32_e32 v135, v135, v255
	ds_write_b128 v154, v[132:135]
	s_branch .LBB7_781
.Lp5_gn_parked:
	ds_read_b128 v[132:135], v154

; __device__ __forceinline__ int fresh_lane() { unsigned z = 0u; asm volatile("" : "+v"(z)); return (int)__builtin_amdgcn_mbcnt_hi(~0u, __builtin_amdgcn_mbcnt_lo(~0u, z)); }
; __device__ __forceinline__ void p7_load(const P& p, int t, int lane, R7& r) {
;     const unsigned char* row = (const unsigned char*)p.out + (size_t)t * 4096; const unsigned char* ys = p.ws + WS_YS3;
;     r.h0 = *(const u32x4*)(row + 32 * lane); r.h1v = *(const u32x4*)(row + 32 * lane + 16); r.y[0] = *(const u32x4*)(row + 2048 + 16 * lane);
; #pragma unroll
;     for (int k = 0; k < 3; ++k) r.y[k + 1] = *(const u32x4*)(ys + ((size_t)t * 3 + k) * DM + 16 * lane);
; }
; __device__ __forceinline__ void p7_finish(const P& p, int t, int lane, const R7& r) {
;     float o[16];
; #pragma unroll
;     for (int q = 0; q < 4; ++q) { o[2 * q] = __uint_as_float(r.h0[q] << 16); o[2 * q + 1] = __uint_as_float(r.h0[q] & 0xffff0000u); o[8 + 2 * q] = __uint_as_float(r.h1v[q] << 16); o[8 + 2 * q + 1] = __uint_as_float(r.h1v[q] & 0xffff0000u); }
; #pragma unroll
;     for (int q = 0; q < 4; ++q) { float s0 = 0.f, s1 = 0.f, s2 = 0.f, s3 = 0.f;
; #pragma unroll
;         for (int k = 0; k < 4; ++k) { const auto lo = __builtin_amdgcn_cvt_pk_f32_fp8((int)r.y[k][q], false), hi = __builtin_amdgcn_cvt_pk_f32_fp8((int)r.y[k][q], true); s0 += lo[0]; s1 += lo[1]; s2 += hi[0]; s3 += hi[1]; }
;         o[4 * q] += s0 * (1.0f / 64.0f); o[4 * q + 1] += s1 * (1.0f / 64.0f); o[4 * q + 2] += s2 * (1.0f / 64.0f); o[4 * q + 3] += s3 * (1.0f / 64.0f); }
;     asm volatile("" ::: "memory");
;     f32x4* dst = (f32x4*)(p.out + (size_t)t * DM + 16 * lane);
; #pragma unroll
;     for (int q = 0; q < 4; ++q) dst[q] = (f32x4){o[4 * q], o[4 * q + 1], o[4 * q + 2], o[4 * q + 3]};
; }
; __device__ __forceinline__ void ph7(const Ctx& c) {
;     const P& p = *c.pp; const int gw = c.bx * NWAVES + c.wave, NGW = c.G * NWAVES, lane = fresh_lane();
;     R7 a, b; int t = gw;
;     if (t < T) p7_load(p, t, lane, a);
;     while (t < T) {
;         const int t1 = t + NGW; if (t1 < T) p7_load(p, t1, lane, b);
;         p7_finish(p, t, lane, a);
;         if (t1 >= T) break;
;         const int t2 = t1 + NGW; if (t2 < T) p7_load(p, t2, lane, a);
;         p7_finish(p, t1, lane, b);
;         t = t2;
;     }
.LBB7_985:
	s_add_i32 s4, s0, s8
	s_cmp_lt_i32 s4, 0x10000
	s_cselect_b64 s[6:7], -1, 0
	s_cmp_gt_i32 s4, 0xffff
	s_cbranch_scc1 .Lp7_skip_b
	s_ashr_i32 s5, s4, 31
	s_lshl_b64 s[10:11], s[4:5], 12
	v_lshl_add_u64 v[32:33], v[54:55], 0, s[10:11]
	global_load_dwordx4 v[12:15], v[32:33], off offset:16 nt
	global_load_dwordx4 v[16:19], v[32:33], off nt
	v_lshl_add_u64 v[32:33], v[32:33], 0, v[48:49]
	v_mad_i64_i32 v[58:59], s[10:11], s4, v56, v[50:51]
	global_load_dwordx4 v[32:35], v[32:33], off offset:2048 nt
	s_nop 0
	global_load_dwordx4 v[36:39], v[58:59], off nt
	global_load_dwordx4 v[40:43], v[58:59], off offset:1024 nt
	global_load_dwordx4 v[44:47], v[58:59], off offset:2048 nt
	s_waitcnt vmcnt(6)
.LBB7_987:
	v_cvt_pk_f32_fp8_sdwa v[60:61], v8 src0_sel:WORD_1
	v_cvt_pk_f32_fp8_sdwa v[64:65], v20 src0_sel:WORD_1
	v_cvt_pk_f32_fp8_e32 v[58:59], v8
	v_cvt_pk_f32_fp8_sdwa v[68:69], v24 src0_sel:WORD_1
	v_cvt_pk_f32_fp8_e32 v[62:63], v20
	v_cvt_pk_f32_fp8_sdwa v[72:73], v28 src0_sel:WORD_1
	v_pk_add_f32 v[60:61], v[60:61], 0 op_sel_hi:[1,0]
	v_cvt_pk_f32_fp8_e32 v[66:67], v24
	v_pk_add_f32 v[60:61], v[60:61], v[64:65]
	v_pk_add_f32 v[58:59], v[58:59], 0 op_sel_hi:[1,0]
	v_pk_add_f32 v[60:61], v[60:61], v[68:69]
	v_cvt_pk_f32_fp8_sdwa v[64:65], v9 src0_sel:WORD_1
	v_cvt_pk_f32_fp8_e32 v[70:71], v28
	v_pk_add_f32 v[58:59], v[58:59], v[62:63]
	v_lshlrev_b32_e32 v62, 16, v5
	v_and_b32_e32 v63, 0xffff0000, v5
	v_pk_add_f32 v[60:61], v[60:61], v[72:73]
	v_cvt_pk_f32_fp8_sdwa v[68:69], v21 src0_sel:WORD_1
	v_pk_fma_f32 v[60:61], v[60:61], s[2:3], v[62:63] op_sel_hi:[1,0,1]
	v_cvt_pk_f32_fp8_e32 v[62:63], v9
	v_cvt_pk_f32_fp8_sdwa v[72:73], v25 src0_sel:WORD_1
	v_pk_add_f32 v[58:59], v[58:59], v[66:67]
	v_cvt_pk_f32_fp8_e32 v[66:67], v21
	v_cvt_pk_f32_fp8_sdwa v[76:77], v29 src0_sel:WORD_1
	v_pk_add_f32 v[64:65], v[64:65], 0 op_sel_hi:[1,0]
	v_pk_add_f32 v[58:59], v[58:59], v[70:71]
	v_cvt_pk_f32_fp8_e32 v[70:71], v25
	v_pk_add_f32 v[64:65], v[64:65], v[68:69]
	v_lshlrev_b32_e32 v74, 16, v4
	v_and_b32_e32 v75, 0xffff0000, v4
	v_pk_add_f32 v[62:63], v[62:63], 0 op_sel_hi:[1,0]
	v_pk_add_f32 v[64:65], v[64:65], v[72:73]
	v_cvt_pk_f32_fp8_sdwa v[68:69], v10 src0_sel:WORD_1
	v_pk_fma_f32 v[58:59], v[58:59], s[2:3], v[74:75] op_sel_hi:[1,0,1]
	v_cvt_pk_f32_fp8_e32 v[74:75], v29
	v_pk_add_f32 v[62:63], v[62:63], v[66:67]
	v_lshlrev_b32_e32 v66, 16, v7
	v_and_b32_e32 v67, 0xffff0000, v7
	v_pk_add_f32 v[64:65], v[64:65], v[76:77]
	v_cvt_pk_f32_fp8_sdwa v[72:73], v22 src0_sel:WORD_1
	v_pk_fma_f32 v[64:65], v[64:65], s[2:3], v[66:67] op_sel_hi:[1,0,1]
	v_cvt_pk_f32_fp8_e32 v[66:67], v10
	v_cvt_pk_f32_fp8_sdwa v[76:77], v26 src0_sel:WORD_1
	v_pk_add_f32 v[62:63], v[62:63], v[70:71]
	v_cvt_pk_f32_fp8_e32 v[70:71], v22
	v_cvt_pk_f32_fp8_sdwa v[80:81], v30 src0_sel:WORD_1
	v_pk_add_f32 v[68:69], v[68:69], 0 op_sel_hi:[1,0]
	v_lshlrev_b32_e32 v78, 16, v6
	v_and_b32_e32 v79, 0xffff0000, v6
	v_pk_add_f32 v[62:63], v[62:63], v[74:75]
	v_cvt_pk_f32_fp8_e32 v[74:75], v26
	v_pk_add_f32 v[68:69], v[68:69], v[72:73]
	v_pk_fma_f32 v[62:63], v[62:63], s[2:3], v[78:79] op_sel_hi:[1,0,1]
	v_cvt_pk_f32_fp8_e32 v[78:79], v30
	v_pk_add_f32 v[66:67], v[66:67], 0 op_sel_hi:[1,0]
	v_pk_add_f32 v[68:69], v[68:69], v[76:77]
	v_pk_add_f32 v[66:67], v[66:67], v[70:71]
	v_lshlrev_b32_e32 v70, 16, v1
	v_and_b32_e32 v71, 0xffff0000, v1
	v_pk_add_f32 v[68:69], v[68:69], v[80:81]
	v_cvt_pk_f32_fp8_sdwa v[72:73], v11 src0_sel:WORD_1
	v_pk_fma_f32 v[68:69], v[68:69], s[2:3], v[70:71] op_sel_hi:[1,0,1]
	v_cvt_pk_f32_fp8_e32 v[70:71], v11
	v_cvt_pk_f32_fp8_sdwa v[76:77], v23 src0_sel:WORD_1
	v_pk_add_f32 v[66:67], v[66:67], v[74:75]
	v_cvt_pk_f32_fp8_e32 v[74:75], v23
	v_cvt_pk_f32_fp8_sdwa v[80:81], v27 src0_sel:WORD_1
	v_lshlrev_b32_e32 v82, 16, v0
	v_and_b32_e32 v83, 0xffff0000, v0
	v_pk_add_f32 v[66:67], v[66:67], v[78:79]
	v_cvt_pk_f32_fp8_e32 v[78:79], v27
	v_cvt_pk_f32_fp8_sdwa v[84:85], v31 src0_sel:WORD_1
	v_pk_fma_f32 v[66:67], v[66:67], s[2:3], v[82:83] op_sel_hi:[1,0,1]
	v_cvt_pk_f32_fp8_e32 v[82:83], v31
	v_pk_add_f32 v[72:73], v[72:73], 0 op_sel_hi:[1,0]
	v_pk_add_f32 v[70:71], v[70:71], 0 op_sel_hi:[1,0]
	v_pk_add_f32 v[72:73], v[72:73], v[76:77]
	v_pk_add_f32 v[70:71], v[70:71], v[74:75]
	v_pk_add_f32 v[72:73], v[72:73], v[80:81]
	s_ashr_i32 s1, s0, 31
	v_pk_add_f32 v[70:71], v[70:71], v[78:79]
	v_lshlrev_b32_e32 v74, 16, v3
	v_and_b32_e32 v75, 0xffff0000, v3
	v_pk_add_f32 v[72:73], v[72:73], v[84:85]
	s_lshl_b64 s[10:11], s[0:1], 12
	v_lshlrev_b32_e32 v86, 16, v2
	v_and_b32_e32 v87, 0xffff0000, v2
	v_pk_add_f32 v[70:71], v[70:71], v[82:83]
	v_pk_fma_f32 v[72:73], v[72:73], s[2:3], v[74:75] op_sel_hi:[1,0,1]
	v_lshl_add_u64 v[74:75], v[52:53], 0, s[10:11]
	s_andn2_b64 vcc, exec, s[6:7]
	s_mov_b64 s[6:7], -1
	v_pk_fma_f32 v[70:71], v[70:71], s[2:3], v[86:87] op_sel_hi:[1,0,1]
	global_store_dwordx4 v[74:75], v[58:61], off
	global_store_dwordx4 v[74:75], v[62:65], off offset:16
	global_store_dwordx4 v[74:75], v[66:69], off offset:32
	global_store_dwordx4 v[74:75], v[70:73], off offset:48
	s_cbranch_vccnz .LBB7_984
	s_add_i32 s0, s3, s0
	s_cmp_gt_i32 s0, 0xffff
	s_cbranch_scc1 .Lp7_skip_a
	s_ashr_i32 s1, s0, 31
	s_lshl_b64 s[6:7], s[0:1], 12
	v_lshl_add_u64 v[8:9], v[54:55], 0, s[6:7]
	global_load_dwordx4 v[0:3], v[8:9], off offset:16 nt
	global_load_dwordx4 v[4:7], v[8:9], off nt
	v_lshl_add_u64 v[8:9], v[8:9], 0, v[48:49]
	v_mad_i64_i32 v[58:59], s[0:1], s0, v56, v[50:51]
	global_load_dwordx4 v[8:11], v[8:9], off offset:2048 nt
	s_nop 0
	global_load_dwordx4 v[20:23], v[58:59], off nt
	global_load_dwordx4 v[24:27], v[58:59], off offset:1024 nt
	global_load_dwordx4 v[28:31], v[58:59], off offset:2048 nt
	s_waitcnt vmcnt(6)
	s_branch .LBB7_983
